# stack16 = stack14 + out-projection first weight fragments requested during A-tile staging and the duplicate accumulator zeroing behind the barrier dropped + expert-phase MFMA loops: first trip peeled
# speedup vs baseline: 1.0117x; 1.0076x over previous
; DEVINL unsigned pk2(float lo, float hi) { const f32x2 v = {lo, hi}; return __builtin_bit_cast(unsigned, __builtin_convertvector(v, bf16v2)); }
; DEVINL float bflo(unsigned u) { return __uint_as_float(u << 16); }
; DEVINL float bfhi(unsigned u) { return __uint_as_float(u & 0xffff0000u); }
; #define LOADB(dst, ks_) do { const unsigned char* ub_ = wb + (size_t)((ks_) * 144) * 1024; \
;         _Pragma("unroll") for (int j_ = 0; j_ < 8; ++j_) dst[j_] = *(const bf16x8*)(ub_ + j_ * 1024 + voff); } while (0)
; #define LOADA(fd, ks_) do { _Pragma("unroll") for (int mi_ = 0; mi_ < 4; ++mi_) fd[mi_] = AFRAG(mi_, ks_); } while (0)
; #define LOADB(dst, ks_) do { const unsigned char* ub_ = wb + (size_t)((ks_) * 64) * 1024; \
;         _Pragma("unroll") for (int j_ = 0; j_ < 8; ++j_) dst[j_] = *(const bf16x8*)(ub_ + j_ * 1024 + voff); } while (0)
; #define LOADA(fd, ks_) do { _Pragma("unroll") for (int mi_ = 0; mi_ < 4; ++mi_) fd[mi_] = AFRAG(mi_, ks_); } while (0)
; DEVINL void phase4(const Params& P, unsigned char* smem) {
;     ...
;             for (int i = 0; i < 16; ++i) {
;                 const int c = (t & 7) + 8 * i;
;                 u32x4 v = *(const u32x4*)(src + c * 8);
;                 const float sc = (c < 64) ? rna : rsw;
;                 v.x = pk2(bflo(v.x) * sc, bfhi(v.x) * sc); v.y = pk2(bflo(v.y) * sc, bfhi(v.y) * sc);
;                 v.z = pk2(bflo(v.z) * sc, bfhi(v.z) * sc); v.w = pk2(bflo(v.w) * sc, bfhi(v.w) * sc);
;                 *(u32x4*)(smem + row * 2048 + ((c ^ (row & 15)) << 4)) = v;
;             }
;     ...
;             bf16x8 fa[4];
;             LOADB(b0, 0); LOADA(fa, 0);
.LBB0_583:
	s_waitcnt vmcnt(8)
	v_mov_b32_e32 v2, v130
	v_mov_b32_e32 v3, v131
	v_mov_b32_e32 v4, v132
	v_mov_b32_e32 v5, v133
	v_mov_b32_e32 v6, v134
	v_mov_b32_e32 v7, v135
	v_mov_b32_e32 v8, v136
	v_mov_b32_e32 v9, v137
	v_mov_b32_e32 v14, v138
	v_mov_b32_e32 v15, v139
	v_mov_b32_e32 v16, v140
	v_mov_b32_e32 v17, v141
	v_mov_b32_e32 v18, v142
	v_mov_b32_e32 v19, v143
	v_mov_b32_e32 v20, v144
	v_mov_b32_e32 v21, v145
	v_mov_b32_e32 v22, v146
	v_mov_b32_e32 v23, v147
	v_mov_b32_e32 v24, v148
	v_mov_b32_e32 v25, v149
	v_mov_b32_e32 v26, v150
	v_mov_b32_e32 v27, v151
	v_mov_b32_e32 v28, v152
	v_mov_b32_e32 v29, v153
	v_mov_b32_e32 v30, v154
	v_mov_b32_e32 v31, v155
	v_mov_b32_e32 v32, v156
	v_mov_b32_e32 v33, v157
	v_mov_b32_e32 v34, v158
	v_mov_b32_e32 v35, v159
	v_mov_b32_e32 v36, v160
	v_mov_b32_e32 v37, v161
	v_lshlrev_b32_e32 v178, 4, v190
	global_load_dwordx4 v[130:133], v178, s[44:45]
	global_load_dwordx4 v[134:137], v178, s[44:45] offset:1024
	global_load_dwordx4 v[138:141], v178, s[44:45] offset:2048
	global_load_dwordx4 v[142:145], v178, s[44:45] offset:3072
	v_add_u32_e32 v240, 0x1000, v178
	global_load_dwordx4 v[158:161], v240, s[44:45]
	global_load_dwordx4 v[154:157], v240, s[44:45] offset:1024
	global_load_dwordx4 v[150:153], v240, s[44:45] offset:2048
	global_load_dwordx4 v[146:149], v240, s[44:45] offset:3072
	v_add_u32_e32 v39, s0, v218
	s_cmp_eq_u32 s0, 0
	v_xor_b32_e32 v40, v39, v220
	v_add_u32_e32 v41, 8, v39
	v_add_u32_e32 v42, 16, v39
	v_add_u32_e32 v43, 24, v39
	v_add_u32_e32 v44, 32, v39
	s_cselect_b64 vcc, -1, 0
	v_add_u32_e32 v45, 40, v39
	v_add_u32_e32 v46, 48, v39
	v_add_u32_e32 v39, 56, v39
	v_lshl_add_u32 v102, v40, 4, v219
	v_xor_b32_e32 v40, v41, v220
	v_xor_b32_e32 v41, v42, v220
	v_xor_b32_e32 v42, v43, v220
	v_xor_b32_e32 v43, v44, v220
	v_cndmask_b32_e32 v38, v13, v12, vcc
	v_xor_b32_e32 v44, v45, v220
	v_xor_b32_e32 v45, v46, v220
	v_xor_b32_e32 v39, v39, v220
	v_lshl_add_u32 v103, v40, 4, v219
	v_lshl_add_u32 v104, v41, 4, v219
	v_lshl_add_u32 v105, v42, 4, v219
	v_lshl_add_u32 v106, v43, 4, v219
	s_add_i32 s0, s0, 64
	v_lshl_add_u32 v107, v44, 4, v219
	v_lshl_add_u32 v108, v45, 4, v219
	v_lshl_add_u64 v[10:11], v[10:11], 0, s[58:59]
	s_cmpk_eq_i32 s0, 0x80
	v_lshl_add_u32 v109, v39, 4, v219
	v_lshlrev_b32_e32 v40, 16, v2
	v_and_b32_e32 v41, 0xffff0000, v2
	v_lshlrev_b32_e32 v2, 16, v3
	v_and_b32_e32 v3, 0xffff0000, v3
	v_lshlrev_b32_e32 v42, 16, v4
	v_and_b32_e32 v43, 0xffff0000, v4
	v_lshlrev_b32_e32 v4, 16, v5
	v_and_b32_e32 v5, 0xffff0000, v5
	v_lshlrev_b32_e32 v44, 16, v6
	v_and_b32_e32 v45, 0xffff0000, v6
	v_lshlrev_b32_e32 v6, 16, v7
	v_and_b32_e32 v7, 0xffff0000, v7
	v_lshlrev_b32_e32 v46, 16, v8
	v_and_b32_e32 v47, 0xffff0000, v8
	v_lshlrev_b32_e32 v8, 16, v9
	v_and_b32_e32 v9, 0xffff0000, v9
	v_lshlrev_b32_e32 v48, 16, v14
	v_and_b32_e32 v49, 0xffff0000, v14
	v_lshlrev_b32_e32 v14, 16, v15
	v_and_b32_e32 v15, 0xffff0000, v15
	v_lshlrev_b32_e32 v50, 16, v16
	v_and_b32_e32 v51, 0xffff0000, v16
	v_lshlrev_b32_e32 v16, 16, v17
	v_and_b32_e32 v17, 0xffff0000, v17
	v_lshlrev_b32_e32 v52, 16, v18
	v_and_b32_e32 v53, 0xffff0000, v18
	v_lshlrev_b32_e32 v18, 16, v19
	v_and_b32_e32 v19, 0xffff0000, v19
	v_lshlrev_b32_e32 v54, 16, v20
	v_and_b32_e32 v55, 0xffff0000, v20
	v_lshlrev_b32_e32 v20, 16, v21
	v_and_b32_e32 v21, 0xffff0000, v21
	v_lshlrev_b32_e32 v56, 16, v22
	v_and_b32_e32 v57, 0xffff0000, v22
	v_lshlrev_b32_e32 v22, 16, v23
	v_and_b32_e32 v23, 0xffff0000, v23
	v_lshlrev_b32_e32 v58, 16, v24
	v_and_b32_e32 v59, 0xffff0000, v24
	v_lshlrev_b32_e32 v24, 16, v25
	v_and_b32_e32 v25, 0xffff0000, v25
	v_lshlrev_b32_e32 v60, 16, v26
	v_and_b32_e32 v61, 0xffff0000, v26
	v_lshlrev_b32_e32 v26, 16, v27
	v_and_b32_e32 v27, 0xffff0000, v27
	v_lshlrev_b32_e32 v62, 16, v28
	v_and_b32_e32 v63, 0xffff0000, v28
	v_lshlrev_b32_e32 v28, 16, v29
	v_and_b32_e32 v29, 0xffff0000, v29
	v_lshlrev_b32_e32 v64, 16, v30
	v_and_b32_e32 v65, 0xffff0000, v30
	v_lshlrev_b32_e32 v30, 16, v31
	v_and_b32_e32 v31, 0xffff0000, v31
	v_lshlrev_b32_e32 v66, 16, v32
	v_and_b32_e32 v67, 0xffff0000, v32
	v_lshlrev_b32_e32 v32, 16, v33
	v_and_b32_e32 v33, 0xffff0000, v33
	v_lshlrev_b32_e32 v68, 16, v34
	v_and_b32_e32 v69, 0xffff0000, v34
	v_lshlrev_b32_e32 v34, 16, v35
	v_and_b32_e32 v35, 0xffff0000, v35
	v_lshlrev_b32_e32 v70, 16, v36
	v_and_b32_e32 v71, 0xffff0000, v36
	v_lshlrev_b32_e32 v36, 16, v37
	v_and_b32_e32 v37, 0xffff0000, v37
	v_pk_mul_f32 v[40:41], v[38:39], v[40:41] op_sel_hi:[0,1]
	v_pk_mul_f32 v[72:73], v[38:39], v[2:3] op_sel_hi:[0,1]
	v_pk_mul_f32 v[42:43], v[38:39], v[42:43] op_sel_hi:[0,1]
	v_pk_mul_f32 v[74:75], v[38:39], v[4:5] op_sel_hi:[0,1]
	v_pk_mul_f32 v[44:45], v[38:39], v[44:45] op_sel_hi:[0,1]
	v_pk_mul_f32 v[76:77], v[38:39], v[6:7] op_sel_hi:[0,1]
	v_pk_mul_f32 v[46:47], v[38:39], v[46:47] op_sel_hi:[0,1]
	v_pk_mul_f32 v[78:79], v[38:39], v[8:9] op_sel_hi:[0,1]
	v_pk_mul_f32 v[48:49], v[38:39], v[48:49] op_sel_hi:[0,1]
	v_pk_mul_f32 v[80:81], v[38:39], v[14:15] op_sel_hi:[0,1]
	v_pk_mul_f32 v[50:51], v[38:39], v[50:51] op_sel_hi:[0,1]
	v_pk_mul_f32 v[82:83], v[38:39], v[16:17] op_sel_hi:[0,1]
	v_pk_mul_f32 v[52:53], v[38:39], v[52:53] op_sel_hi:[0,1]
	v_pk_mul_f32 v[84:85], v[38:39], v[18:19] op_sel_hi:[0,1]
	v_pk_mul_f32 v[54:55], v[38:39], v[54:55] op_sel_hi:[0,1]
	v_pk_mul_f32 v[86:87], v[38:39], v[20:21] op_sel_hi:[0,1]
	v_pk_mul_f32 v[56:57], v[38:39], v[56:57] op_sel_hi:[0,1]
	v_pk_mul_f32 v[88:89], v[38:39], v[22:23] op_sel_hi:[0,1]
	v_pk_mul_f32 v[58:59], v[38:39], v[58:59] op_sel_hi:[0,1]
	v_pk_mul_f32 v[90:91], v[38:39], v[24:25] op_sel_hi:[0,1]
	v_pk_mul_f32 v[60:61], v[38:39], v[60:61] op_sel_hi:[0,1]
; DEVINL unsigned pk2(float lo, float hi) { const f32x2 v = {lo, hi}; return __builtin_bit_cast(unsigned, __builtin_convertvector(v, bf16v2)); }
; DEVINL float bflo(unsigned u) { return __uint_as_float(u << 16); }
; DEVINL float bfhi(unsigned u) { return __uint_as_float(u & 0xffff0000u); }
; DEVINL void phase4(const Params& P, unsigned char* smem) {
;     ...
;             for (int i = 0; i < 16; ++i) {
;                 const int c = (t & 7) + 8 * i;
;                 u32x4 v = *(const u32x4*)(src + c * 8);
;                 const float sc = (c < 64) ? rna : rsw;
;                 v.x = pk2(bflo(v.x) * sc, bfhi(v.x) * sc); v.y = pk2(bflo(v.y) * sc, bfhi(v.y) * sc);
;                 v.z = pk2(bflo(v.z) * sc, bfhi(v.z) * sc); v.w = pk2(bflo(v.w) * sc, bfhi(v.w) * sc);
;                 *(u32x4*)(smem + row * 2048 + ((c ^ (row & 15)) << 4)) = v;
;             }
	v_pk_mul_f32 v[92:93], v[38:39], v[26:27] op_sel_hi:[0,1]
	v_pk_mul_f32 v[62:63], v[38:39], v[62:63] op_sel_hi:[0,1]
	v_pk_mul_f32 v[94:95], v[38:39], v[28:29] op_sel_hi:[0,1]
	v_pk_mul_f32 v[64:65], v[38:39], v[64:65] op_sel_hi:[0,1]
	v_pk_mul_f32 v[96:97], v[38:39], v[30:31] op_sel_hi:[0,1]
	v_pk_mul_f32 v[66:67], v[38:39], v[66:67] op_sel_hi:[0,1]
	v_pk_mul_f32 v[98:99], v[38:39], v[32:33] op_sel_hi:[0,1]
	v_pk_mul_f32 v[68:69], v[38:39], v[68:69] op_sel_hi:[0,1]
	v_pk_mul_f32 v[100:101], v[38:39], v[34:35] op_sel_hi:[0,1]
	v_pk_mul_f32 v[70:71], v[38:39], v[70:71] op_sel_hi:[0,1]
	v_pk_mul_f32 v[38:39], v[38:39], v[36:37] op_sel_hi:[0,1]
	v_cvt_pk_bf16_f32 v2, v40, v41
	v_cvt_pk_bf16_f32 v3, v72, v73
	v_cvt_pk_bf16_f32 v4, v42, v43
	v_cvt_pk_bf16_f32 v5, v74, v75
	v_cvt_pk_bf16_f32 v6, v44, v45
	v_cvt_pk_bf16_f32 v7, v76, v77
	v_cvt_pk_bf16_f32 v8, v46, v47
	v_cvt_pk_bf16_f32 v9, v78, v79
	v_cvt_pk_bf16_f32 v14, v48, v49
	v_cvt_pk_bf16_f32 v15, v80, v81
	v_cvt_pk_bf16_f32 v16, v50, v51
	v_cvt_pk_bf16_f32 v17, v82, v83
	v_cvt_pk_bf16_f32 v18, v52, v53
	v_cvt_pk_bf16_f32 v19, v84, v85
	v_cvt_pk_bf16_f32 v20, v54, v55
	v_cvt_pk_bf16_f32 v21, v86, v87
	v_cvt_pk_bf16_f32 v22, v56, v57
	v_cvt_pk_bf16_f32 v23, v88, v89
	v_cvt_pk_bf16_f32 v24, v58, v59
	v_cvt_pk_bf16_f32 v25, v90, v91
	v_cvt_pk_bf16_f32 v26, v60, v61
	v_cvt_pk_bf16_f32 v27, v92, v93
	v_cvt_pk_bf16_f32 v28, v62, v63
	v_cvt_pk_bf16_f32 v29, v94, v95
	v_cvt_pk_bf16_f32 v30, v64, v65
	v_cvt_pk_bf16_f32 v31, v96, v97
	v_cvt_pk_bf16_f32 v32, v66, v67
	v_cvt_pk_bf16_f32 v33, v98, v99
	v_cvt_pk_bf16_f32 v34, v68, v69
	v_cvt_pk_bf16_f32 v35, v100, v101
	v_cvt_pk_bf16_f32 v36, v70, v71
	v_cvt_pk_bf16_f32 v37, v38, v39
	ds_write_b128 v102, v[2:5]
	ds_write_b128 v103, v[6:9]
	ds_write_b128 v104, v[14:17]
	ds_write_b128 v105, v[18:21]
	ds_write_b128 v106, v[22:25]
	ds_write_b128 v107, v[26:29]
	ds_write_b128 v108, v[30:33]
	ds_write_b128 v109, v[34:37]
	s_waitcnt vmcnt(8)
	v_mov_b32_e32 v2, v162
	v_mov_b32_e32 v3, v163
	v_mov_b32_e32 v4, v164
	v_mov_b32_e32 v5, v165
	v_mov_b32_e32 v6, v166
	v_mov_b32_e32 v7, v167
	v_mov_b32_e32 v8, v168
	v_mov_b32_e32 v9, v169
	v_mov_b32_e32 v14, v170
	v_mov_b32_e32 v15, v171
	v_mov_b32_e32 v16, v172
	v_mov_b32_e32 v17, v173
	v_mov_b32_e32 v18, v174
	v_mov_b32_e32 v19, v175
	v_mov_b32_e32 v20, v176
	v_mov_b32_e32 v21, v177
	v_mov_b32_e32 v22, v196
	v_mov_b32_e32 v23, v197
	v_mov_b32_e32 v24, v198
	v_mov_b32_e32 v25, v199
	v_mov_b32_e32 v26, v200
	v_mov_b32_e32 v27, v201
	v_mov_b32_e32 v28, v202
	v_mov_b32_e32 v29, v203
	v_mov_b32_e32 v30, v204
	v_mov_b32_e32 v31, v205
	v_mov_b32_e32 v32, v206
	v_mov_b32_e32 v33, v207
	v_mov_b32_e32 v34, v208
	v_mov_b32_e32 v35, v209
	v_mov_b32_e32 v36, v210
	v_mov_b32_e32 v37, v211
	v_add_u32_e32 v39, s0, v218
	s_cmp_eq_u32 s0, 0
	v_xor_b32_e32 v40, v39, v220
	v_add_u32_e32 v41, 8, v39
	v_add_u32_e32 v42, 16, v39
	v_add_u32_e32 v43, 24, v39
	v_add_u32_e32 v44, 32, v39
	s_cselect_b64 vcc, -1, 0
	v_add_u32_e32 v45, 40, v39
	v_add_u32_e32 v46, 48, v39
	v_add_u32_e32 v39, 56, v39
	v_lshl_add_u32 v102, v40, 4, v219
	v_xor_b32_e32 v40, v41, v220
	v_xor_b32_e32 v41, v42, v220
	v_xor_b32_e32 v42, v43, v220
	v_xor_b32_e32 v43, v44, v220
	v_cndmask_b32_e32 v38, v13, v12, vcc
	v_xor_b32_e32 v44, v45, v220
	v_xor_b32_e32 v45, v46, v220
	v_xor_b32_e32 v39, v39, v220
	v_lshl_add_u32 v103, v40, 4, v219
	v_lshl_add_u32 v104, v41, 4, v219
	v_lshl_add_u32 v105, v42, 4, v219
	v_lshl_add_u32 v106, v43, 4, v219
	s_add_i32 s0, s0, 64
	v_lshl_add_u32 v107, v44, 4, v219
	v_lshl_add_u32 v108, v45, 4, v219
	v_lshl_add_u64 v[10:11], v[10:11], 0, s[58:59]
	s_cmpk_eq_i32 s0, 0x80
	v_lshl_add_u32 v109, v39, 4, v219
	v_lshlrev_b32_e32 v40, 16, v2
	v_and_b32_e32 v41, 0xffff0000, v2
	v_lshlrev_b32_e32 v2, 16, v3
	v_and_b32_e32 v3, 0xffff0000, v3
	v_lshlrev_b32_e32 v42, 16, v4
	v_and_b32_e32 v43, 0xffff0000, v4
	v_lshlrev_b32_e32 v4, 16, v5
	v_and_b32_e32 v5, 0xffff0000, v5
	v_lshlrev_b32_e32 v44, 16, v6
	v_and_b32_e32 v45, 0xffff0000, v6
	v_lshlrev_b32_e32 v6, 16, v7
	v_and_b32_e32 v7, 0xffff0000, v7
	v_lshlrev_b32_e32 v46, 16, v8
	v_and_b32_e32 v47, 0xffff0000, v8
	v_lshlrev_b32_e32 v8, 16, v9
	v_and_b32_e32 v9, 0xffff0000, v9
	v_lshlrev_b32_e32 v48, 16, v14
	v_and_b32_e32 v49, 0xffff0000, v14
	v_lshlrev_b32_e32 v14, 16, v15
	v_and_b32_e32 v15, 0xffff0000, v15
	v_lshlrev_b32_e32 v50, 16, v16
	v_and_b32_e32 v51, 0xffff0000, v16
	v_lshlrev_b32_e32 v16, 16, v17
	v_and_b32_e32 v17, 0xffff0000, v17
	v_lshlrev_b32_e32 v52, 16, v18
	v_and_b32_e32 v53, 0xffff0000, v18
	v_lshlrev_b32_e32 v18, 16, v19
	v_and_b32_e32 v19, 0xffff0000, v19
	v_lshlrev_b32_e32 v54, 16, v20
	v_and_b32_e32 v55, 0xffff0000, v20
	v_lshlrev_b32_e32 v20, 16, v21
	v_and_b32_e32 v21, 0xffff0000, v21
	v_lshlrev_b32_e32 v56, 16, v22
	v_and_b32_e32 v57, 0xffff0000, v22
	v_lshlrev_b32_e32 v22, 16, v23
	v_and_b32_e32 v23, 0xffff0000, v23
	v_lshlrev_b32_e32 v58, 16, v24
	v_and_b32_e32 v59, 0xffff0000, v24
	v_lshlrev_b32_e32 v24, 16, v25
	v_and_b32_e32 v25, 0xffff0000, v25
	v_lshlrev_b32_e32 v60, 16, v26
	v_and_b32_e32 v61, 0xffff0000, v26
	v_lshlrev_b32_e32 v26, 16, v27
	v_and_b32_e32 v27, 0xffff0000, v27
	v_lshlrev_b32_e32 v62, 16, v28
	v_and_b32_e32 v63, 0xffff0000, v28
	v_lshlrev_b32_e32 v28, 16, v29
	v_and_b32_e32 v29, 0xffff0000, v29
	v_lshlrev_b32_e32 v64, 16, v30
	v_and_b32_e32 v65, 0xffff0000, v30
	v_lshlrev_b32_e32 v30, 16, v31
	v_and_b32_e32 v31, 0xffff0000, v31
	v_lshlrev_b32_e32 v66, 16, v32
	v_and_b32_e32 v67, 0xffff0000, v32
	v_lshlrev_b32_e32 v32, 16, v33
	v_and_b32_e32 v33, 0xffff0000, v33
	v_lshlrev_b32_e32 v68, 16, v34
	v_and_b32_e32 v69, 0xffff0000, v34
	v_lshlrev_b32_e32 v34, 16, v35
; DEVINL unsigned pk2(float lo, float hi) { const f32x2 v = {lo, hi}; return __builtin_bit_cast(unsigned, __builtin_convertvector(v, bf16v2)); }
; DEVINL float bflo(unsigned u) { return __uint_as_float(u << 16); }
; DEVINL float bfhi(unsigned u) { return __uint_as_float(u & 0xffff0000u); }
; DEVINL void phase4(const Params& P, unsigned char* smem) {
;     ...
;             for (int i = 0; i < 16; ++i) {
;                 const int c = (t & 7) + 8 * i;
;                 u32x4 v = *(const u32x4*)(src + c * 8);
;                 const float sc = (c < 64) ? rna : rsw;
;                 v.x = pk2(bflo(v.x) * sc, bfhi(v.x) * sc); v.y = pk2(bflo(v.y) * sc, bfhi(v.y) * sc);
;                 v.z = pk2(bflo(v.z) * sc, bfhi(v.z) * sc); v.w = pk2(bflo(v.w) * sc, bfhi(v.w) * sc);
;                 *(u32x4*)(smem + row * 2048 + ((c ^ (row & 15)) << 4)) = v;
;             }
;         }
;         __syncthreads();
;         f32x4 acc[8][4];
; #pragma unroll
;         for (int i = 0; i < 8; ++i)
; #pragma unroll
;             for (int mi = 0; mi < 4; ++mi) acc[i][mi] = (f32x4){0.f, 0.f, 0.f, 0.f};
	v_and_b32_e32 v35, 0xffff0000, v35
	v_lshlrev_b32_e32 v70, 16, v36
	v_and_b32_e32 v71, 0xffff0000, v36
	v_lshlrev_b32_e32 v36, 16, v37
	v_and_b32_e32 v37, 0xffff0000, v37
	v_pk_mul_f32 v[40:41], v[38:39], v[40:41] op_sel_hi:[0,1]
	v_pk_mul_f32 v[72:73], v[38:39], v[2:3] op_sel_hi:[0,1]
	v_pk_mul_f32 v[42:43], v[38:39], v[42:43] op_sel_hi:[0,1]
	v_pk_mul_f32 v[74:75], v[38:39], v[4:5] op_sel_hi:[0,1]
	v_pk_mul_f32 v[44:45], v[38:39], v[44:45] op_sel_hi:[0,1]
	v_pk_mul_f32 v[76:77], v[38:39], v[6:7] op_sel_hi:[0,1]
	v_pk_mul_f32 v[46:47], v[38:39], v[46:47] op_sel_hi:[0,1]
	v_pk_mul_f32 v[78:79], v[38:39], v[8:9] op_sel_hi:[0,1]
	v_pk_mul_f32 v[48:49], v[38:39], v[48:49] op_sel_hi:[0,1]
	v_pk_mul_f32 v[80:81], v[38:39], v[14:15] op_sel_hi:[0,1]
	v_pk_mul_f32 v[50:51], v[38:39], v[50:51] op_sel_hi:[0,1]
	v_pk_mul_f32 v[82:83], v[38:39], v[16:17] op_sel_hi:[0,1]
	v_pk_mul_f32 v[52:53], v[38:39], v[52:53] op_sel_hi:[0,1]
	v_pk_mul_f32 v[84:85], v[38:39], v[18:19] op_sel_hi:[0,1]
	v_pk_mul_f32 v[54:55], v[38:39], v[54:55] op_sel_hi:[0,1]
	v_pk_mul_f32 v[86:87], v[38:39], v[20:21] op_sel_hi:[0,1]
	v_pk_mul_f32 v[56:57], v[38:39], v[56:57] op_sel_hi:[0,1]
	v_pk_mul_f32 v[88:89], v[38:39], v[22:23] op_sel_hi:[0,1]
	v_pk_mul_f32 v[58:59], v[38:39], v[58:59] op_sel_hi:[0,1]
	v_pk_mul_f32 v[90:91], v[38:39], v[24:25] op_sel_hi:[0,1]
	v_pk_mul_f32 v[60:61], v[38:39], v[60:61] op_sel_hi:[0,1]
	v_pk_mul_f32 v[92:93], v[38:39], v[26:27] op_sel_hi:[0,1]
	v_pk_mul_f32 v[62:63], v[38:39], v[62:63] op_sel_hi:[0,1]
	v_pk_mul_f32 v[94:95], v[38:39], v[28:29] op_sel_hi:[0,1]
	v_pk_mul_f32 v[64:65], v[38:39], v[64:65] op_sel_hi:[0,1]
	v_pk_mul_f32 v[96:97], v[38:39], v[30:31] op_sel_hi:[0,1]
	v_pk_mul_f32 v[66:67], v[38:39], v[66:67] op_sel_hi:[0,1]
	v_pk_mul_f32 v[98:99], v[38:39], v[32:33] op_sel_hi:[0,1]
	v_pk_mul_f32 v[68:69], v[38:39], v[68:69] op_sel_hi:[0,1]
	v_pk_mul_f32 v[100:101], v[38:39], v[34:35] op_sel_hi:[0,1]
	v_pk_mul_f32 v[70:71], v[38:39], v[70:71] op_sel_hi:[0,1]
	v_pk_mul_f32 v[38:39], v[38:39], v[36:37] op_sel_hi:[0,1]
	v_cvt_pk_bf16_f32 v2, v40, v41
	v_cvt_pk_bf16_f32 v3, v72, v73
	v_cvt_pk_bf16_f32 v4, v42, v43
	v_cvt_pk_bf16_f32 v5, v74, v75
	v_cvt_pk_bf16_f32 v6, v44, v45
	v_cvt_pk_bf16_f32 v7, v76, v77
	v_cvt_pk_bf16_f32 v8, v46, v47
	v_cvt_pk_bf16_f32 v9, v78, v79
	v_cvt_pk_bf16_f32 v14, v48, v49
	v_cvt_pk_bf16_f32 v15, v80, v81
	v_cvt_pk_bf16_f32 v16, v50, v51
	v_cvt_pk_bf16_f32 v17, v82, v83
	v_cvt_pk_bf16_f32 v18, v52, v53
	v_cvt_pk_bf16_f32 v19, v84, v85
	v_cvt_pk_bf16_f32 v20, v54, v55
	v_cvt_pk_bf16_f32 v21, v86, v87
	v_cvt_pk_bf16_f32 v22, v56, v57
	v_cvt_pk_bf16_f32 v23, v88, v89
	v_cvt_pk_bf16_f32 v24, v58, v59
	v_cvt_pk_bf16_f32 v25, v90, v91
	v_cvt_pk_bf16_f32 v26, v60, v61
	v_cvt_pk_bf16_f32 v27, v92, v93
	v_cvt_pk_bf16_f32 v28, v62, v63
	v_cvt_pk_bf16_f32 v29, v94, v95
	v_cvt_pk_bf16_f32 v30, v64, v65
	v_cvt_pk_bf16_f32 v31, v96, v97
	v_cvt_pk_bf16_f32 v32, v66, v67
	v_cvt_pk_bf16_f32 v33, v98, v99
	v_cvt_pk_bf16_f32 v34, v68, v69
	v_cvt_pk_bf16_f32 v35, v100, v101
	v_cvt_pk_bf16_f32 v36, v70, v71
	v_cvt_pk_bf16_f32 v37, v38, v39
	ds_write_b128 v102, v[2:5]
	ds_write_b128 v103, v[6:9]
	ds_write_b128 v104, v[14:17]
	ds_write_b128 v105, v[18:21]
	ds_write_b128 v106, v[22:25]
	ds_write_b128 v107, v[26:29]
	ds_write_b128 v108, v[30:33]
	ds_write_b128 v109, v[34:37]
	v_mov_b32_e32 v5, 0
	v_and_b32_e32 v238, 15, v190
	v_ashrrev_i32_e32 v204, 4, v190
	s_and_b64 vcc, exec, s[42:43]
	v_mov_b32_e32 v4, v5
	v_mov_b32_e32 v3, v5
	v_mov_b32_e32 v2, v5
	v_mov_b32_e32 v9, v5
	v_mov_b32_e32 v8, v5
	v_mov_b32_e32 v7, v5
	v_mov_b32_e32 v6, v5
	v_mov_b32_e32 v69, v5
	v_mov_b32_e32 v68, v5
	v_mov_b32_e32 v67, v5
	v_mov_b32_e32 v66, v5
	v_mov_b32_e32 v73, v5
	v_mov_b32_e32 v72, v5
	v_mov_b32_e32 v71, v5
	v_mov_b32_e32 v70, v5
	v_mov_b32_e32 v13, v5
	v_mov_b32_e32 v12, v5
	v_mov_b32_e32 v11, v5
	v_mov_b32_e32 v10, v5
	v_mov_b32_e32 v17, v5
	v_mov_b32_e32 v16, v5
	v_mov_b32_e32 v15, v5
	v_mov_b32_e32 v14, v5
	v_mov_b32_e32 v77, v5
	v_mov_b32_e32 v76, v5
	v_mov_b32_e32 v75, v5
	v_mov_b32_e32 v74, v5
	v_mov_b32_e32 v81, v5
	v_mov_b32_e32 v80, v5
	v_mov_b32_e32 v79, v5
	v_mov_b32_e32 v78, v5
	v_mov_b32_e32 v21, v5
	v_mov_b32_e32 v20, v5
	v_mov_b32_e32 v19, v5
	v_mov_b32_e32 v18, v5
	v_mov_b32_e32 v25, v5
	v_mov_b32_e32 v24, v5
	v_mov_b32_e32 v23, v5
	v_mov_b32_e32 v22, v5
	v_mov_b32_e32 v85, v5
	v_mov_b32_e32 v84, v5
	v_mov_b32_e32 v83, v5
	v_mov_b32_e32 v82, v5
	v_mov_b32_e32 v89, v5
	v_mov_b32_e32 v88, v5
	v_mov_b32_e32 v87, v5
	v_mov_b32_e32 v86, v5
	v_mov_b32_e32 v29, v5
	v_mov_b32_e32 v28, v5
	v_mov_b32_e32 v27, v5
	v_mov_b32_e32 v26, v5
	v_mov_b32_e32 v33, v5
	v_mov_b32_e32 v32, v5
	v_mov_b32_e32 v31, v5
	v_mov_b32_e32 v30, v5
	v_mov_b32_e32 v93, v5
	v_mov_b32_e32 v92, v5
	v_mov_b32_e32 v91, v5
	v_mov_b32_e32 v90, v5
	v_mov_b32_e32 v97, v5
	v_mov_b32_e32 v96, v5
	v_mov_b32_e32 v95, v5
	v_mov_b32_e32 v94, v5
	v_mov_b32_e32 v129, v5
	v_mov_b32_e32 v128, v5
	v_mov_b32_e32 v127, v5
	v_mov_b32_e32 v126, v5
	v_mov_b32_e32 v125, v5
	v_mov_b32_e32 v124, v5
	v_mov_b32_e32 v123, v5
	v_mov_b32_e32 v122, v5
	v_mov_b32_e32 v65, v5
	v_mov_b32_e32 v64, v5
	v_mov_b32_e32 v63, v5
	v_mov_b32_e32 v62, v5
	v_mov_b32_e32 v61, v5
	v_mov_b32_e32 v60, v5
	v_mov_b32_e32 v59, v5
	v_mov_b32_e32 v58, v5
	v_mov_b32_e32 v121, v5
	v_mov_b32_e32 v120, v5
	v_mov_b32_e32 v119, v5
	v_mov_b32_e32 v118, v5
	v_mov_b32_e32 v117, v5
	v_mov_b32_e32 v116, v5
	v_mov_b32_e32 v115, v5
	v_mov_b32_e32 v114, v5
	v_mov_b32_e32 v57, v5
	v_mov_b32_e32 v56, v5
	v_mov_b32_e32 v55, v5
	v_mov_b32_e32 v54, v5
	v_mov_b32_e32 v53, v5
	v_mov_b32_e32 v52, v5
	v_mov_b32_e32 v51, v5
	v_mov_b32_e32 v50, v5
	v_mov_b32_e32 v113, v5
	v_mov_b32_e32 v112, v5
	v_mov_b32_e32 v111, v5
	v_mov_b32_e32 v110, v5
	v_mov_b32_e32 v109, v5
	v_mov_b32_e32 v108, v5
	v_mov_b32_e32 v107, v5
	v_mov_b32_e32 v106, v5
	v_mov_b32_e32 v49, v5
	v_mov_b32_e32 v48, v5
	v_mov_b32_e32 v47, v5
	v_mov_b32_e32 v46, v5
	v_mov_b32_e32 v45, v5
	v_mov_b32_e32 v44, v5
	v_mov_b32_e32 v43, v5
	v_mov_b32_e32 v42, v5
	v_mov_b32_e32 v105, v5
	v_mov_b32_e32 v104, v5
	v_mov_b32_e32 v103, v5
	v_mov_b32_e32 v102, v5
	v_mov_b32_e32 v101, v5
	v_mov_b32_e32 v100, v5
	v_mov_b32_e32 v99, v5
	v_mov_b32_e32 v98, v5
	v_mov_b32_e32 v41, v5
	v_mov_b32_e32 v40, v5
	v_mov_b32_e32 v39, v5
	v_mov_b32_e32 v38, v5
	v_mov_b32_e32 v37, v5
	v_mov_b32_e32 v36, v5
	v_mov_b32_e32 v35, v5
	v_mov_b32_e32 v34, v5
	s_waitcnt lgkmcnt(0)
	s_barrier
; #define LOADB(dst, ks_) do { const unsigned char* ub_ = wb + (size_t)((ks_) * 144) * 1024; \
;         _Pragma("unroll") for (int j_ = 0; j_ < 8; ++j_) dst[j_] = *(const bf16x8*)(ub_ + j_ * 1024 + voff); } while (0)
; #define LOADA(fd, ks_) do { _Pragma("unroll") for (int mi_ = 0; mi_ < 4; ++mi_) fd[mi_] = AFRAG(mi_, ks_); } while (0)
; #define LOADB(dst, ks_) do { const unsigned char* ub_ = wb + (size_t)((ks_) * 64) * 1024; \
;         _Pragma("unroll") for (int j_ = 0; j_ < 8; ++j_) dst[j_] = *(const bf16x8*)(ub_ + j_ * 1024 + voff); } while (0)
; #define LOADA(fd, ks_) do { _Pragma("unroll") for (int mi_ = 0; mi_ < 4; ++mi_) fd[mi_] = AFRAG(mi_, ks_); } while (0)
; DEVINL void phase4(const Params& P, unsigned char* smem) {
;     ...
;             const unsigned char* wb = (const unsigned char*)(P.ws + WS_WOF) + (size_t)(8 * wv) * 1024;
;             unsigned voff = (unsigned)(lane * 16);
;             asm volatile("" : "+v"(voff));
;             const int aoff = lr * 2048;
;     ...
;             bf16x8 b0[8], b1[8];
;     ...
;             bf16x8 fa[4];
;             LOADB(b0, 0); LOADA(fa, 0);
	s_cbranch_vccz .LBB0_587
	v_lshl_add_u64 v[192:193], s[44:45], 0, v[178:179]
	v_lshl_add_u32 v191, v238, 11, 0
	v_xor_b32_e32 v2, v204, v238
	v_lshl_add_u32 v2, v2, 4, v191
	v_add_u32_e32 v3, 0x10000, v2
	ds_read_b128 v[174:177], v2
	ds_read_b128 v[170:173], v2 offset:32768
	v_add_u32_e32 v2, 0x18000, v2
	ds_read_b128 v[166:169], v3
	ds_read_b128 v[162:165], v2
	s_mov_b32 s0, 0
	v_add_u32_e32 v196, 4, v204
	v_lshl_add_u64 v[194:195], s[52:53], 0, v[178:179]
	v_mov_b32_e32 v2, 0
	v_mov_b32_e32 v3, 0
	s_mov_b64 s[8:9], 0x1000
	v_lshl_add_u64 v[194:195], v[194:195], 0, s[8:9]
	global_load_dwordx4 v[198:201], v[194:195], off offset:-4096
	global_load_dwordx4 v[206:209], v[194:195], off offset:-3072
	global_load_dwordx4 v[210:213], v[194:195], off offset:-2048
	global_load_dwordx4 v[240:243], v[194:195], off offset:-1024
	global_load_dwordx4 v[244:247], v[194:195], off
	global_load_dwordx4 v[248:251], v[194:195], off offset:1024
	global_load_dwordx4 v[226:229], v[194:195], off offset:2048
	global_load_dwordx4 v[230:233], v[194:195], off offset:3072

; #define MX(a_, b_, c_) __builtin_amdgcn_mfma_scale_f32_16x16x128_f8f6f4(a_, b_, c_, 0, 0, 0, 0x7f7f7f7f, 0, 0x7f7f7f7f)
; #define LD32(p_) CAT8(*(const i32x4v*)(p_), *(const i32x4v*)((p_) + 16))
; #define AFRAG(mi_, ks_) CAT8(*(const i32x4v*)(smem + aoff + (mi_) * 16384 + (((8 * (ks_) + 2 * g) ^ lr) << 4)), *(const i32x4v*)(smem + aoff + (mi_) * 16384 + (((8 * (ks_) + 2 * g + 1) ^ lr) << 4)))
; #define AFRAG(hb_, mi_, ks_) CAT8(*(const i32x4v*)((hb_) + aoff + (mi_) * 4096 + (((8 * (ks_) + 2 * g2) ^ lr2) << 4)), *(const i32x4v*)((hb_) + aoff + (mi_) * 4096 + (((8 * (ks_) + 2 * g2 + 1) ^ lr2) << 4)))
; DEVINL void phase5(const Params& P, unsigned char* smem) {
;     ...
;         for (int sx = 0; sx < 2; ++sx) {
;             const int e = sx ? e_hi : e_lo;
;             f32x4 acc[4][5];
; #pragma unroll
;             for (int i = 0; i < 4; ++i)
; #pragma unroll
;                 for (int mi = 0; mi < 5; ++mi) acc[i][mi] = (f32x4){0.f, 0.f, 0.f, 0.f};
;             const unsigned char* wb1 = P.ws + WS_WGUF + (size_t)e * (8 * 32 * 2048) + (size_t)(4 * wv) * 2048;
;             const int aoff = lr * 1024;
;     ...
;             const unsigned char* nxt_ = sx ? P.ws + WS_WDF + (size_t)e_lo * (2 * 64 * 2048) + (size_t)(8 * wv) * 2048 : P.ws + WS_WGUF + (size_t)e_hi * (8 * 32 * 2048) + (size_t)(4 * wv) * 2048;
; #pragma unroll 1
;             for (int ks = 0; ks < 8; ++ks) {
;                 i32x8 fa[5];
; #pragma unroll
;                 for (int mi_ = 0; mi_ < 5; ++mi_) fa[mi_] = AFRAG(mi_, ks);
;                 const unsigned char* un_ = ks + 1 < 8 ? wb1 + (size_t)((ks + 1) * 32) * 2048 : nxt_;
; #pragma unroll
;                 for (int j_ = 0; j_ < 4; ++j_) {
; #pragma unroll
;                     for (int mi_ = 0; mi_ < 5; ++mi_) acc[j_][mi_] = MX(b0[j_], fa[mi_], acc[j_][mi_]);
;                     b0[j_] = LD32(un_ + j_ * 2048 + voff);
;                     __builtin_amdgcn_sched_barrier(0);
;                 }
;             }
.LBB0_721:
	s_xor_b64 s[28:29], s[30:31], -1
	s_and_b64 s[34:35], s[30:31], exec
	s_cselect_b32 s34, s49, s0
	s_ashr_i32 s35, s34, 31
	s_lshl_b64 s[34:35], s[34:35], 19
	s_and_b64 s[54:55], s[30:31], exec
	s_cselect_b32 s54, s52, s50
	s_cselect_b32 s55, s51, s1
	s_add_u32 s56, s41, s34
	s_addc_u32 s57, s42, s35
	s_mov_b64 s[34:35], 0
	v_mov_b32_e32 v118, v116
	s_waitcnt vmcnt(11)
	s_waitcnt vmcnt(8)
	v_add_u32_e32 v120, 1, v118
	v_xor_b32_e32 v119, v118, v114
	v_xor_b32_e32 v120, v120, v114
	v_lshlrev_b32_e32 v119, 4, v119
	v_lshlrev_b32_e32 v152, 4, v120
	v_add_u32_e32 v140, v115, v119
	v_add_u32_e32 v148, v115, v152
	v_add_u32_e32 v119, v117, v119
	v_add_u32_e32 v156, v117, v152
	ds_read_b128 v[120:123], v140
	ds_read_b128 v[128:131], v140 offset:16384
	ds_read_b128 v[124:127], v148
	ds_read_b128 v[132:135], v148 offset:16384
	ds_read_b128 v[136:139], v140 offset:32768
	ds_read_b128 v[144:147], v140 offset:49152
	ds_read_b128 v[140:143], v148 offset:32768
	ds_read_b128 v[148:151], v148 offset:49152
	s_add_u32 s58, s56, s34
	ds_read_b128 v[152:155], v119
	ds_read_b128 v[156:159], v156
	s_addc_u32 s59, s57, s35
	s_cmp_eq_u32 s34, 0x70000
	s_cselect_b32 s59, s54, s59
	s_cselect_b32 s58, s55, s58
	v_lshl_add_u64 v[160:161], s[58:59], 0, v[194:195]
	s_waitcnt vmcnt(6) lgkmcnt(7)
	v_mfma_scale_f32_16x16x128_f8f6f4 v[110:113], v[2:9], v[120:127], 0, v220, v220 op_sel_hi:[0,0,0]
	s_waitcnt lgkmcnt(6)
	v_mfma_scale_f32_16x16x128_f8f6f4 v[102:105], v[2:9], v[128:135], 0, v220, v220 op_sel_hi:[0,0,0]
	s_waitcnt lgkmcnt(3)
	v_mfma_scale_f32_16x16x128_f8f6f4 v[94:97], v[2:9], v[136:143], 0, v220, v220 op_sel_hi:[0,0,0]
	s_waitcnt lgkmcnt(2)
	v_mfma_scale_f32_16x16x128_f8f6f4 v[86:89], v[2:9], v[144:151], 0, v220, v220 op_sel_hi:[0,0,0]
	s_waitcnt lgkmcnt(0)
	v_mfma_scale_f32_16x16x128_f8f6f4 v[78:81], v[2:9], v[152:159], 0, v220, v220 op_sel_hi:[0,0,0]
	global_load_dwordx4 v[2:5], v[160:161], off
	global_load_dwordx4 v[6:9], v[160:161], off offset:16
	s_waitcnt vmcnt(6)
	v_mfma_scale_f32_16x16x128_f8f6f4 v[106:109], v[10:17], v[120:127], 0, v220, v220 op_sel_hi:[0,0,0]
	v_mfma_scale_f32_16x16x128_f8f6f4 v[98:101], v[10:17], v[128:135], 0, v220, v220 op_sel_hi:[0,0,0]
	v_mfma_scale_f32_16x16x128_f8f6f4 v[90:93], v[10:17], v[136:143], 0, v220, v220 op_sel_hi:[0,0,0]
	v_mfma_scale_f32_16x16x128_f8f6f4 v[82:85], v[10:17], v[144:151], 0, v220, v220 op_sel_hi:[0,0,0]
	v_mfma_scale_f32_16x16x128_f8f6f4 v[74:77], v[10:17], v[152:159], 0, v220, v220 op_sel_hi:[0,0,0]
	global_load_dwordx4 v[10:13], v[160:161], off offset:2048
	global_load_dwordx4 v[14:17], v[160:161], off offset:2064
	v_add_co_u32_e32 v164, vcc, s45, v160
	s_waitcnt vmcnt(6)
	v_mfma_scale_f32_16x16x128_f8f6f4 v[70:73], v[18:25], v[120:127], 0, v220, v220 op_sel_hi:[0,0,0]
	v_addc_co_u32_e32 v165, vcc, 0, v161, vcc
	v_lshl_add_u64 v[162:163], v[160:161], 0, s[14:15]
	v_mfma_scale_f32_16x16x128_f8f6f4 v[62:65], v[18:25], v[128:135], 0, v220, v220 op_sel_hi:[0,0,0]
	v_mfma_scale_f32_16x16x128_f8f6f4 v[54:57], v[18:25], v[136:143], 0, v220, v220 op_sel_hi:[0,0,0]
	v_mfma_scale_f32_16x16x128_f8f6f4 v[46:49], v[18:25], v[144:151], 0, v220, v220 op_sel_hi:[0,0,0]
	v_mfma_scale_f32_16x16x128_f8f6f4 v[34:37], v[18:25], v[152:159], 0, v220, v220 op_sel_hi:[0,0,0]
	global_load_dwordx4 v[18:21], v[164:165], off
	global_load_dwordx4 v[22:25], v[162:163], off offset:16
	s_waitcnt vmcnt(6)
	v_mfma_scale_f32_16x16x128_f8f6f4 v[66:69], v[26:33], v[120:127], 0, v220, v220 op_sel_hi:[0,0,0]
	v_lshl_add_u64 v[120:121], v[160:161], 0, s[16:17]
	v_mfma_scale_f32_16x16x128_f8f6f4 v[58:61], v[26:33], v[128:135], 0, v220, v220 op_sel_hi:[0,0,0]
	v_mfma_scale_f32_16x16x128_f8f6f4 v[50:53], v[26:33], v[136:143], 0, v220, v220 op_sel_hi:[0,0,0]
	v_mfma_scale_f32_16x16x128_f8f6f4 v[38:41], v[26:33], v[144:151], 0, v220, v220 op_sel_hi:[0,0,0]
	v_mfma_scale_f32_16x16x128_f8f6f4 v[42:45], v[26:33], v[152:159], 0, v220, v220 op_sel_hi:[0,0,0]
	global_load_dwordx4 v[26:29], v[164:165], off offset:2048
	global_load_dwordx4 v[30:33], v[120:121], off offset:16
	s_add_u32 s34, s34, 0x10000
	s_addc_u32 s35, s35, 0
	s_cmp_eq_u32 s34, 0x80000
	v_add_u32_e32 v118, 8, v118
.LBB0_722:
	v_add_u32_e32 v120, 1, v118
	v_xor_b32_e32 v119, v118, v114
	v_xor_b32_e32 v120, v120, v114
	v_lshlrev_b32_e32 v119, 4, v119
	v_lshlrev_b32_e32 v152, 4, v120
	v_add_u32_e32 v140, v115, v119
	v_add_u32_e32 v148, v115, v152
	v_add_u32_e32 v119, v117, v119
	v_add_u32_e32 v156, v117, v152
	ds_read_b128 v[120:123], v140
	ds_read_b128 v[128:131], v140 offset:16384
	ds_read_b128 v[124:127], v148
	ds_read_b128 v[132:135], v148 offset:16384
	ds_read_b128 v[136:139], v140 offset:32768
	ds_read_b128 v[144:147], v140 offset:49152
	ds_read_b128 v[140:143], v148 offset:32768
	ds_read_b128 v[148:151], v148 offset:49152
	s_add_u32 s58, s56, s34
	ds_read_b128 v[152:155], v119
	ds_read_b128 v[156:159], v156
	s_addc_u32 s59, s57, s35
	s_cmp_eq_u32 s34, 0x70000
	s_cselect_b32 s59, s54, s59
	s_cselect_b32 s58, s55, s58
	v_lshl_add_u64 v[160:161], s[58:59], 0, v[194:195]
	s_waitcnt vmcnt(6) lgkmcnt(7)
	v_mfma_scale_f32_16x16x128_f8f6f4 v[110:113], v[2:9], v[120:127], v[110:113], v220, v220 op_sel_hi:[0,0,0]
	s_waitcnt lgkmcnt(6)
	v_mfma_scale_f32_16x16x128_f8f6f4 v[102:105], v[2:9], v[128:135], v[102:105], v220, v220 op_sel_hi:[0,0,0]
	s_waitcnt lgkmcnt(3)
	v_mfma_scale_f32_16x16x128_f8f6f4 v[94:97], v[2:9], v[136:143], v[94:97], v220, v220 op_sel_hi:[0,0,0]
	s_waitcnt lgkmcnt(2)
	v_mfma_scale_f32_16x16x128_f8f6f4 v[86:89], v[2:9], v[144:151], v[86:89], v220, v220 op_sel_hi:[0,0,0]
	s_waitcnt lgkmcnt(0)
; DEVINL float sat8(float v) { return __builtin_amdgcn_fmed3f(v, -448.f, 448.f); }
; #define MX(a_, b_, c_) __builtin_amdgcn_mfma_scale_f32_16x16x128_f8f6f4(a_, b_, c_, 0, 0, 0, 0x7f7f7f7f, 0, 0x7f7f7f7f)
; #define LD32(p_) CAT8(*(const i32x4v*)(p_), *(const i32x4v*)((p_) + 16))
; #define AFRAG(mi_, ks_) CAT8(*(const i32x4v*)(smem + aoff + (mi_) * 16384 + (((8 * (ks_) + 2 * g) ^ lr) << 4)), *(const i32x4v*)(smem + aoff + (mi_) * 16384 + (((8 * (ks_) + 2 * g + 1) ^ lr) << 4)))
; #define AFRAG(hb_, mi_, ks_) CAT8(*(const i32x4v*)((hb_) + aoff + (mi_) * 4096 + (((8 * (ks_) + 2 * g2) ^ lr2) << 4)), *(const i32x4v*)((hb_) + aoff + (mi_) * 4096 + (((8 * (ks_) + 2 * g2 + 1) ^ lr2) << 4)))
; DEVINL void phase5(const Params& P, unsigned char* smem) {
;     ...
;             for (int ks = 0; ks < 8; ++ks) {
;                 i32x8 fa[5];
; #pragma unroll
;                 for (int mi_ = 0; mi_ < 5; ++mi_) fa[mi_] = AFRAG(mi_, ks);
;                 const unsigned char* un_ = ks + 1 < 8 ? wb1 + (size_t)((ks + 1) * 32) * 2048 : nxt_;
; #pragma unroll
;                 for (int j_ = 0; j_ < 4; ++j_) {
; #pragma unroll
;                     for (int mi_ = 0; mi_ < 5; ++mi_) acc[j_][mi_] = MX(b0[j_], fa[mi_], acc[j_][mi_]);
;                     b0[j_] = LD32(un_ + j_ * 2048 + voff);
;                     __builtin_amdgcn_sched_barrier(0);
;                 }
;             }
;     ...
;             int l1 = lane;
;             asm volatile("" : "+v"(l1));
;             const int lrh = l1 & 15, gh = l1 >> 4;
;             unsigned char* hsm = hs0 + sx * 20480;
;             const float* swt = sx ? s_wh : s_wl;
; #pragma unroll
;             for (int p = 0; p < 2; ++p)
; #pragma unroll
;                 for (int mi = 0; mi < 5; ++mi) {
;                     const int row = 16 * mi + lrh, c16 = 2 * wv + p;
;                     const float ws_ = swt[row] * (8.f / 32.f);
;                     const f32x4 gt = acc[2 * p][mi] * (1.f / 32.f), up = acc[2 * p + 1][mi] * ws_;
;                     const unsigned o = pk4_fp8(sat8(gt.x * __builtin_amdgcn_rcpf(1.f + __expf(-gt.x)) * up.x), sat8(gt.y * __builtin_amdgcn_rcpf(1.f + __expf(-gt.y)) * up.y), sat8(gt.z * __builtin_amdgcn_rcpf(1.f + __expf(-gt.z)) * up.z), sat8(gt.w * __builtin_amdgcn_rcpf(1.f + __expf(-gt.w)) * up.w));
;                     *(unsigned*)(hsm + row * 256 + ((c16 ^ (row & 15)) << 4) + 4 * gh) = o;
	v_mfma_scale_f32_16x16x128_f8f6f4 v[78:81], v[2:9], v[152:159], v[78:81], v220, v220 op_sel_hi:[0,0,0]
	global_load_dwordx4 v[2:5], v[160:161], off
	global_load_dwordx4 v[6:9], v[160:161], off offset:16
	s_waitcnt vmcnt(6)
	v_mfma_scale_f32_16x16x128_f8f6f4 v[106:109], v[10:17], v[120:127], v[106:109], v220, v220 op_sel_hi:[0,0,0]
	v_mfma_scale_f32_16x16x128_f8f6f4 v[98:101], v[10:17], v[128:135], v[98:101], v220, v220 op_sel_hi:[0,0,0]
	v_mfma_scale_f32_16x16x128_f8f6f4 v[90:93], v[10:17], v[136:143], v[90:93], v220, v220 op_sel_hi:[0,0,0]
	v_mfma_scale_f32_16x16x128_f8f6f4 v[82:85], v[10:17], v[144:151], v[82:85], v220, v220 op_sel_hi:[0,0,0]
	v_mfma_scale_f32_16x16x128_f8f6f4 v[74:77], v[10:17], v[152:159], v[74:77], v220, v220 op_sel_hi:[0,0,0]
	global_load_dwordx4 v[10:13], v[160:161], off offset:2048
	global_load_dwordx4 v[14:17], v[160:161], off offset:2064
	v_add_co_u32_e32 v164, vcc, s45, v160
	s_waitcnt vmcnt(6)
	v_mfma_scale_f32_16x16x128_f8f6f4 v[70:73], v[18:25], v[120:127], v[70:73], v220, v220 op_sel_hi:[0,0,0]
	v_addc_co_u32_e32 v165, vcc, 0, v161, vcc
	v_lshl_add_u64 v[162:163], v[160:161], 0, s[14:15]
	v_mfma_scale_f32_16x16x128_f8f6f4 v[62:65], v[18:25], v[128:135], v[62:65], v220, v220 op_sel_hi:[0,0,0]
	v_mfma_scale_f32_16x16x128_f8f6f4 v[54:57], v[18:25], v[136:143], v[54:57], v220, v220 op_sel_hi:[0,0,0]
	v_mfma_scale_f32_16x16x128_f8f6f4 v[46:49], v[18:25], v[144:151], v[46:49], v220, v220 op_sel_hi:[0,0,0]
	v_mfma_scale_f32_16x16x128_f8f6f4 v[34:37], v[18:25], v[152:159], v[34:37], v220, v220 op_sel_hi:[0,0,0]
	global_load_dwordx4 v[18:21], v[164:165], off
	global_load_dwordx4 v[22:25], v[162:163], off offset:16
	s_waitcnt vmcnt(6)
	v_mfma_scale_f32_16x16x128_f8f6f4 v[66:69], v[26:33], v[120:127], v[66:69], v220, v220 op_sel_hi:[0,0,0]
	v_lshl_add_u64 v[120:121], v[160:161], 0, s[16:17]
	v_mfma_scale_f32_16x16x128_f8f6f4 v[58:61], v[26:33], v[128:135], v[58:61], v220, v220 op_sel_hi:[0,0,0]
	v_mfma_scale_f32_16x16x128_f8f6f4 v[50:53], v[26:33], v[136:143], v[50:53], v220, v220 op_sel_hi:[0,0,0]
	v_mfma_scale_f32_16x16x128_f8f6f4 v[38:41], v[26:33], v[144:151], v[38:41], v220, v220 op_sel_hi:[0,0,0]
	v_mfma_scale_f32_16x16x128_f8f6f4 v[42:45], v[26:33], v[152:159], v[42:45], v220, v220 op_sel_hi:[0,0,0]
	global_load_dwordx4 v[26:29], v[164:165], off offset:2048
	global_load_dwordx4 v[30:33], v[120:121], off offset:16
	s_add_u32 s34, s34, 0x10000
	s_addc_u32 s35, s35, 0
	s_cmp_eq_u32 s34, 0x80000
	v_add_u32_e32 v118, 8, v118
	s_cbranch_scc0 .LBB0_722
	s_add_i32 s34, s53, 0
	s_add_i32 s34, s34, 0x14000
	s_and_b64 s[30:31], s[30:31], exec
	v_mov_b32_e32 v122, v223
	s_cselect_b32 s30, 0x24a40, s44
	s_add_i32 s30, s30, 0
	v_and_b32_e32 v123, 15, v122
	v_ashrrev_i32_e32 v118, 2, v122
	v_and_b32_e32 v118, -4, v118
	v_lshl_add_u32 v125, v123, 2, s30
	v_add_u32_e32 v124, s34, v118
	ds_read2_b32 v[118:119], v125 offset1:16
	v_pk_mul_f32 v[120:121], v[110:111], s[18:19] op_sel_hi:[1,0]
	v_pk_mul_f32 v[112:113], v[112:113], s[18:19] op_sel_hi:[1,0]
	v_mul_f32_e32 v110, 0xbfb8aa3b, v120
	v_exp_f32_e32 v111, v110
	s_waitcnt lgkmcnt(0)
	v_mul_f32_e32 v110, 0x3e800000, v118
	v_mul_f32_e32 v118, 0xbfb8aa3b, v121
	v_exp_f32_e32 v118, v118
	v_pk_mul_f32 v[108:109], v[108:109], v[110:111] op_sel_hi:[1,0]
	v_add_f32_e32 v111, 1.0, v111
	v_rcp_f32_e32 v111, v111
	v_bitop3_b32 v126, v122, s19, 15 bitop3:0x6c
	v_pk_mul_f32 v[104:105], v[104:105], s[18:19] op_sel_hi:[1,0]
	v_pk_mul_f32 v[96:97], v[96:97], s[18:19] op_sel_hi:[1,0]
	v_pk_mul_f32 v[106:107], v[106:107], v[110:111] op_sel_hi:[1,0]
	v_mul_f32_e32 v111, v120, v111
	v_mul_f32_e32 v106, v111, v106
	v_add_f32_e32 v111, 1.0, v118
	v_rcp_f32_e32 v111, v111
	v_mul_f32_e32 v118, 0xbfb8aa3b, v112
	v_exp_f32_e32 v118, v118
	v_med3_f32 v106, v106, s46, v222
	v_mul_f32_e32 v111, v121, v111
	v_mul_f32_e32 v107, v111, v107
	v_add_f32_e32 v111, 1.0, v118
	v_rcp_f32_e32 v111, v111
	v_mul_f32_e32 v118, 0xbfb8aa3b, v113
	v_exp_f32_e32 v118, v118
	v_med3_f32 v107, v107, s46, v222
	v_mul_f32_e32 v111, v112, v111
	v_mul_f32_e32 v108, v111, v108
	v_add_f32_e32 v111, 1.0, v118
	v_rcp_f32_e32 v111, v111
	v_mov_b32_e32 v112, 0
	v_cvt_pk_fp8_f32 v112, v106, v107
	v_med3_f32 v108, v108, s46, v222
	v_mul_f32_e32 v106, v113, v111
	v_mul_f32_e32 v106, v106, v109
	v_med3_f32 v106, v106, s46, v222
	v_cvt_pk_fp8_f32 v112, v108, v106 op_sel:[0,0,1]
	v_lshl_add_u32 v108, v126, 4, v124
	v_lshlrev_b32_e32 v109, 8, v123
	v_add_u32_e32 v106, v108, v109
	ds_write_b32 v106, v112
	v_pk_mul_f32 v[106:107], v[102:103], s[18:19] op_sel_hi:[1,0]
	v_pk_mul_f32 v[88:89], v[88:89], s[18:19] op_sel_hi:[1,0]
	v_mul_f32_e32 v102, 0xbfb8aa3b, v106
	v_exp_f32_e32 v103, v102
	v_mul_f32_e32 v102, 0x3e800000, v119
	v_mul_f32_e32 v111, 0xbfb8aa3b, v107
	v_exp_f32_e32 v111, v111
	v_pk_mul_f32 v[100:101], v[100:101], v[102:103] op_sel_hi:[1,0]
	v_add_f32_e32 v103, 1.0, v103
	v_rcp_f32_e32 v103, v103
	v_pk_mul_f32 v[80:81], v[80:81], s[18:19] op_sel_hi:[1,0]
	v_pk_mul_f32 v[70:71], v[70:71], s[18:19] op_sel_hi:[1,0]
	v_pk_mul_f32 v[66:67], v[66:67], v[110:111] op_sel_hi:[1,0]
	v_pk_mul_f32 v[98:99], v[98:99], v[102:103] op_sel_hi:[1,0]
	v_mul_f32_e32 v103, v106, v103
	v_mul_f32_e32 v98, v103, v98
	v_add_f32_e32 v103, 1.0, v111
	v_rcp_f32_e32 v103, v103
	v_mul_f32_e32 v106, 0xbfb8aa3b, v104
	v_exp_f32_e32 v106, v106
	v_med3_f32 v98, v98, s46, v222
	v_mul_f32_e32 v103, v107, v103
	v_mul_f32_e32 v99, v103, v99
	v_add_f32_e32 v103, 1.0, v106
	v_rcp_f32_e32 v103, v103
	v_mul_f32_e32 v106, 0xbfb8aa3b, v105
	v_exp_f32_e32 v106, v106
	v_med3_f32 v99, v99, s46, v222
	v_mul_f32_e32 v103, v104, v103
	v_mul_f32_e32 v100, v103, v100
	v_add_f32_e32 v103, 1.0, v106
	v_rcp_f32_e32 v103, v103
	v_mov_b32_e32 v104, 0
	v_cvt_pk_fp8_f32 v104, v98, v99
	v_med3_f32 v100, v100, s46, v222
	v_mul_f32_e32 v98, v105, v103
	v_mul_f32_e32 v98, v98, v101
	v_med3_f32 v98, v98, s46, v222
	v_cvt_pk_fp8_f32 v104, v100, v98 op_sel:[0,0,1]
	ds_read2_b32 v[98:99], v125 offset0:32 offset1:48
	v_pk_mul_f32 v[100:101], v[94:95], s[18:19] op_sel_hi:[1,0]
	v_pk_mul_f32 v[72:73], v[72:73], s[18:19] op_sel_hi:[1,0]
	v_mul_f32_e32 v94, 0xbfb8aa3b, v100
	v_exp_f32_e32 v95, v94
	s_waitcnt lgkmcnt(0)
; DEVINL float sat8(float v) { return __builtin_amdgcn_fmed3f(v, -448.f, 448.f); }
; DEVINL void phase5(const Params& P, unsigned char* smem) {
;     ...
;             const float* swt = sx ? s_wh : s_wl;
; #pragma unroll
;             for (int p = 0; p < 2; ++p)
; #pragma unroll
;                 for (int mi = 0; mi < 5; ++mi) {
;                     const int row = 16 * mi + lrh, c16 = 2 * wv + p;
;                     const float ws_ = swt[row] * (8.f / 32.f);
;                     const f32x4 gt = acc[2 * p][mi] * (1.f / 32.f), up = acc[2 * p + 1][mi] * ws_;
;                     const unsigned o = pk4_fp8(sat8(gt.x * __builtin_amdgcn_rcpf(1.f + __expf(-gt.x)) * up.x), sat8(gt.y * __builtin_amdgcn_rcpf(1.f + __expf(-gt.y)) * up.y), sat8(gt.z * __builtin_amdgcn_rcpf(1.f + __expf(-gt.z)) * up.z), sat8(gt.w * __builtin_amdgcn_rcpf(1.f + __expf(-gt.w)) * up.w));
;                     *(unsigned*)(hsm + row * 256 + ((c16 ^ (row & 15)) << 4) + 4 * gh) = o;
	v_mul_f32_e32 v94, 0x3e800000, v98
	v_mul_f32_e32 v98, 0xbfb8aa3b, v101
	v_exp_f32_e32 v98, v98
	v_pk_mul_f32 v[92:93], v[92:93], v[94:95] op_sel_hi:[1,0]
	v_add_f32_e32 v95, 1.0, v95
	v_rcp_f32_e32 v95, v95
	v_pk_mul_f32 v[68:69], v[68:69], v[110:111] op_sel_hi:[1,0]
	v_or_b32_e32 v103, 0x1000, v109
	v_add_u32_e32 v105, v108, v103
	v_pk_mul_f32 v[90:91], v[90:91], v[94:95] op_sel_hi:[1,0]
	v_mul_f32_e32 v95, v100, v95
	v_mul_f32_e32 v90, v95, v90
	v_add_f32_e32 v95, 1.0, v98
	v_rcp_f32_e32 v95, v95
	v_mul_f32_e32 v98, 0xbfb8aa3b, v96
	v_exp_f32_e32 v98, v98
	v_med3_f32 v90, v90, s46, v222
	v_mul_f32_e32 v95, v101, v95
	v_mul_f32_e32 v91, v95, v91
	v_add_f32_e32 v95, 1.0, v98
	v_rcp_f32_e32 v95, v95
	v_mul_f32_e32 v98, 0xbfb8aa3b, v97
	v_exp_f32_e32 v98, v98
	v_med3_f32 v91, v91, s46, v222
	v_mul_f32_e32 v95, v96, v95
	v_mul_f32_e32 v92, v95, v92
	v_add_f32_e32 v95, 1.0, v98
	v_rcp_f32_e32 v95, v95
	v_mov_b32_e32 v96, 0
	v_cvt_pk_fp8_f32 v96, v90, v91
	v_med3_f32 v92, v92, s46, v222
	v_mul_f32_e32 v90, v97, v95
	v_mul_f32_e32 v90, v90, v93
	v_med3_f32 v90, v90, s46, v222
	v_cvt_pk_fp8_f32 v96, v92, v90 op_sel:[0,0,1]
	v_or_b32_e32 v92, 0x2000, v109
	v_add_u32_e32 v90, v108, v92
	v_pk_mul_f32 v[62:63], v[62:63], s[18:19] op_sel_hi:[1,0]
	ds_write_b32 v90, v96
	v_pk_mul_f32 v[90:91], v[86:87], s[18:19] op_sel_hi:[1,0]
	ds_write_b32 v105, v104
	v_mul_f32_e32 v86, 0xbfb8aa3b, v90
	v_exp_f32_e32 v87, v86
	v_mul_f32_e32 v86, 0x3e800000, v99
	v_mul_f32_e32 v93, 0xbfb8aa3b, v91
	v_exp_f32_e32 v93, v93
	v_pk_mul_f32 v[84:85], v[84:85], v[86:87] op_sel_hi:[1,0]
	v_add_f32_e32 v87, 1.0, v87
	v_rcp_f32_e32 v87, v87
	v_pk_mul_f32 v[58:59], v[58:59], v[102:103] op_sel_hi:[1,0]
	v_pk_mul_f32 v[64:65], v[64:65], s[18:19] op_sel_hi:[1,0]
	v_pk_mul_f32 v[60:61], v[60:61], v[102:103] op_sel_hi:[1,0]
	v_pk_mul_f32 v[82:83], v[82:83], v[86:87] op_sel_hi:[1,0]
	v_mul_f32_e32 v87, v90, v87
	v_mul_f32_e32 v82, v87, v82
	v_add_f32_e32 v87, 1.0, v93
	v_rcp_f32_e32 v87, v87
	v_mul_f32_e32 v90, 0xbfb8aa3b, v88
	v_exp_f32_e32 v90, v90
	v_med3_f32 v82, v82, s46, v222
	v_mul_f32_e32 v87, v91, v87
	v_mul_f32_e32 v83, v87, v83
	v_add_f32_e32 v87, 1.0, v90
	v_rcp_f32_e32 v87, v87
	v_mul_f32_e32 v90, 0xbfb8aa3b, v89
	v_exp_f32_e32 v90, v90
	v_med3_f32 v83, v83, s46, v222
	v_mul_f32_e32 v87, v88, v87
	v_mul_f32_e32 v84, v87, v84
	v_add_f32_e32 v87, 1.0, v90
	v_rcp_f32_e32 v87, v87
	v_mov_b32_e32 v88, 0
	v_cvt_pk_fp8_f32 v88, v82, v83
	v_med3_f32 v84, v84, s46, v222
	v_mul_f32_e32 v82, v89, v87
	v_mul_f32_e32 v82, v82, v85
	v_med3_f32 v82, v82, s46, v222
	v_cvt_pk_fp8_f32 v88, v84, v82 op_sel:[0,0,1]
	v_or_b32_e32 v84, 0x3000, v109
	v_add_u32_e32 v82, v108, v84
	ds_read_b32 v85, v125 offset:256
	ds_write_b32 v82, v88
	v_pk_mul_f32 v[82:83], v[78:79], s[18:19] op_sel_hi:[1,0]
	v_pk_mul_f32 v[54:55], v[54:55], s[18:19] op_sel_hi:[1,0]
	v_mul_f32_e32 v78, 0xbfb8aa3b, v82
	v_exp_f32_e32 v79, v78
	s_waitcnt lgkmcnt(1)
	v_mul_f32_e32 v78, 0x3e800000, v85
	v_mul_f32_e32 v85, 0xbfb8aa3b, v83
	v_exp_f32_e32 v85, v85
	v_pk_mul_f32 v[76:77], v[76:77], v[78:79] op_sel_hi:[1,0]
	v_add_f32_e32 v79, 1.0, v79
	v_rcp_f32_e32 v79, v79
	v_pk_mul_f32 v[50:51], v[50:51], v[94:95] op_sel_hi:[1,0]
	v_pk_mul_f32 v[56:57], v[56:57], s[18:19] op_sel_hi:[1,0]
	v_pk_mul_f32 v[52:53], v[52:53], v[94:95] op_sel_hi:[1,0]
	v_pk_mul_f32 v[74:75], v[74:75], v[78:79] op_sel_hi:[1,0]
	v_mul_f32_e32 v79, v82, v79
	v_mul_f32_e32 v74, v79, v74
	v_add_f32_e32 v79, 1.0, v85
	v_rcp_f32_e32 v79, v79
	v_mul_f32_e32 v82, 0xbfb8aa3b, v80
	v_exp_f32_e32 v82, v82
	v_med3_f32 v74, v74, s46, v222
	v_mul_f32_e32 v79, v83, v79
	v_mul_f32_e32 v75, v79, v75
	v_add_f32_e32 v79, 1.0, v82
	v_rcp_f32_e32 v79, v79
	v_mul_f32_e32 v82, 0xbfb8aa3b, v81
	v_exp_f32_e32 v82, v82
	v_med3_f32 v75, v75, s46, v222
	v_mul_f32_e32 v79, v80, v79
	v_mul_f32_e32 v76, v79, v76
	v_add_f32_e32 v79, 1.0, v82
	v_rcp_f32_e32 v79, v79
	v_mov_b32_e32 v80, 0
	v_cvt_pk_fp8_f32 v80, v74, v75
	v_med3_f32 v76, v76, s46, v222
	v_mul_f32_e32 v74, v81, v79
	v_mul_f32_e32 v74, v74, v77
	v_med3_f32 v74, v74, s46, v222
	v_cvt_pk_fp8_f32 v80, v76, v74 op_sel:[0,0,1]
	v_mul_f32_e32 v76, 0xbfb8aa3b, v70
	v_exp_f32_e32 v76, v76
	v_or_b32_e32 v74, 0x4000, v109
	v_add_u32_e32 v75, v108, v74
	ds_write_b32 v75, v80
	v_add_f32_e32 v75, 1.0, v76
	v_rcp_f32_e32 v75, v75
	v_mul_f32_e32 v76, 0xbfb8aa3b, v71
	v_exp_f32_e32 v76, v76
	v_pk_mul_f32 v[46:47], v[46:47], s[18:19] op_sel_hi:[1,0]
	v_mul_f32_e32 v70, v70, v75
	v_mul_f32_e32 v66, v70, v66
	v_add_f32_e32 v70, 1.0, v76
	v_rcp_f32_e32 v70, v70
	v_mul_f32_e32 v75, 0xbfb8aa3b, v72
	v_exp_f32_e32 v75, v75
	v_med3_f32 v66, v66, s46, v222
	v_mul_f32_e32 v70, v71, v70
	v_mul_f32_e32 v67, v70, v67
	v_add_f32_e32 v70, 1.0, v75
	v_rcp_f32_e32 v70, v70
	v_mul_f32_e32 v71, 0xbfb8aa3b, v73
	v_exp_f32_e32 v71, v71
	v_med3_f32 v67, v67, s46, v222
	v_mul_f32_e32 v70, v72, v70
	v_mul_f32_e32 v68, v70, v68
	v_add_f32_e32 v70, 1.0, v71
	v_rcp_f32_e32 v70, v70
	v_mov_b32_e32 v71, 0
	v_cvt_pk_fp8_f32 v71, v66, v67
	v_med3_f32 v68, v68, s46, v222
	v_mul_f32_e32 v66, v73, v70
	v_mul_f32_e32 v66, v66, v69
	v_med3_f32 v66, v66, s46, v222
	v_cvt_pk_fp8_f32 v71, v68, v66 op_sel:[0,0,1]
	v_bitop3_b32 v66, v122, s36, 15 bitop3:0x6c
	v_lshl_add_u32 v66, v66, 4, v124
	v_add_u32_e32 v67, v66, v109
	ds_write_b32 v67, v71
	v_mul_f32_e32 v67, 0xbfb8aa3b, v62
	v_exp_f32_e32 v67, v67
	v_mul_f32_e32 v68, 0xbfb8aa3b, v63
	v_exp_f32_e32 v68, v68
	v_pk_mul_f32 v[38:39], v[38:39], v[86:87] op_sel_hi:[1,0]
	v_add_f32_e32 v67, 1.0, v67
	v_rcp_f32_e32 v67, v67
	v_add_f32_e32 v68, 1.0, v68
	v_rcp_f32_e32 v68, v68
	v_pk_mul_f32 v[48:49], v[48:49], s[18:19] op_sel_hi:[1,0]
; DEVINL float sat8(float v) { return __builtin_amdgcn_fmed3f(v, -448.f, 448.f); }
; #define MX(a_, b_, c_) __builtin_amdgcn_mfma_scale_f32_16x16x128_f8f6f4(a_, b_, c_, 0, 0, 0, 0x7f7f7f7f, 0, 0x7f7f7f7f)
; #define LD32(p_) CAT8(*(const i32x4v*)(p_), *(const i32x4v*)((p_) + 16))
; DEVINL void phase5(const Params& P, unsigned char* smem) {
;     ...
;             for (int p = 0; p < 2; ++p)
; #pragma unroll
;                 for (int mi = 0; mi < 5; ++mi) {
;                     const int row = 16 * mi + lrh, c16 = 2 * wv + p;
;                     const float ws_ = swt[row] * (8.f / 32.f);
;                     const f32x4 gt = acc[2 * p][mi] * (1.f / 32.f), up = acc[2 * p + 1][mi] * ws_;
;                     const unsigned o = pk4_fp8(sat8(gt.x * __builtin_amdgcn_rcpf(1.f + __expf(-gt.x)) * up.x), sat8(gt.y * __builtin_amdgcn_rcpf(1.f + __expf(-gt.y)) * up.y), sat8(gt.z * __builtin_amdgcn_rcpf(1.f + __expf(-gt.z)) * up.z), sat8(gt.w * __builtin_amdgcn_rcpf(1.f + __expf(-gt.w)) * up.w));
;                     *(unsigned*)(hsm + row * 256 + ((c16 ^ (row & 15)) << 4) + 4 * gh) = o;
;                 }
;         }
;         __syncthreads();
;     ...
;             for (int ph = 0; ph < 2; ++ph) {
; #pragma unroll
;                 for (int i = 0; i < 4; ++i)
; #pragma unroll
;                     for (int mi = 0; mi < 5; ++mi) acc[i][mi] = (f32x4){0.f, 0.f, 0.f, 0.f};
; #pragma unroll 1
;                 for (int sk = 0; sk < 4; ++sk) {
;                     const int sn = 4 * ph + sk + 1 < 8 ? 4 * ph + sk + 1 : 7, sxn = (sn >> 1) & 1;
;                     const unsigned char* wn = wd0 + (size_t)(sxn ? e_hi : e_lo) * (2 * 64 * 2048) + (size_t)((sn & 1) * 64 + 4 * (sn >> 2)) * 2048;
;                     const unsigned char* hb = hs0 + (sk >> 1) * 20480;
;                     i32x8 fa[5];
; #pragma unroll
;                     for (int mi_ = 0; mi_ < 5; ++mi_) fa[mi_] = AFRAG(hb, mi_, sk & 1);
; #pragma unroll
;                     for (int j_ = 0; j_ < 4; ++j_) {
; #pragma unroll
;                         for (int mi_ = 0; mi_ < 5; ++mi_) acc[j_][mi_] = MX(b0[j_], fa[mi_], acc[j_][mi_]);
;                         b0[j_] = LD32(wn + j_ * 2048 + voff2);
;                         __builtin_amdgcn_sched_barrier(0);
;                     }
	v_mul_f32_e32 v62, v62, v67
	v_mul_f32_e32 v58, v62, v58
	v_mul_f32_e32 v62, v63, v68
	v_mul_f32_e32 v59, v62, v59
	v_mul_f32_e32 v62, 0xbfb8aa3b, v65
	v_exp_f32_e32 v62, v62
	v_med3_f32 v58, v58, s46, v222
	v_med3_f32 v59, v59, s46, v222
	v_mul_f32_e32 v63, 0xbfb8aa3b, v64
	v_add_f32_e32 v62, 1.0, v62
	v_rcp_f32_e32 v62, v62
	v_exp_f32_e32 v63, v63
	v_pk_mul_f32 v[40:41], v[40:41], v[86:87] op_sel_hi:[1,0]
	v_pk_mul_f32 v[34:35], v[34:35], s[18:19] op_sel_hi:[1,0]
	v_mul_f32_e32 v62, v65, v62
	v_mul_f32_e32 v61, v62, v61
	v_mov_b32_e32 v62, 0
	v_cvt_pk_fp8_f32 v62, v58, v59
	v_mul_f32_e32 v58, 0xbfb8aa3b, v54
	v_exp_f32_e32 v58, v58
	v_mul_f32_e32 v59, 0xbfb8aa3b, v55
	v_exp_f32_e32 v59, v59
	v_add_f32_e32 v63, 1.0, v63
	v_add_f32_e32 v58, 1.0, v58
	v_rcp_f32_e32 v58, v58
	v_rcp_f32_e32 v63, v63
	v_med3_f32 v61, v61, s46, v222
	v_pk_mul_f32 v[36:37], v[36:37], s[18:19] op_sel_hi:[1,0]
	v_mul_f32_e32 v54, v54, v58
	v_mul_f32_e32 v50, v54, v50
	v_add_f32_e32 v54, 1.0, v59
	v_rcp_f32_e32 v54, v54
	v_mul_f32_e32 v58, 0xbfb8aa3b, v56
	v_exp_f32_e32 v58, v58
	v_med3_f32 v50, v50, s46, v222
	v_mul_f32_e32 v54, v55, v54
	v_mul_f32_e32 v51, v54, v51
	v_add_f32_e32 v54, 1.0, v58
	v_rcp_f32_e32 v54, v54
	v_mul_f32_e32 v55, 0xbfb8aa3b, v57
	v_exp_f32_e32 v55, v55
	v_med3_f32 v51, v51, s46, v222
	v_mul_f32_e32 v54, v56, v54
	v_mul_f32_e32 v52, v54, v52
	v_add_f32_e32 v54, 1.0, v55
	v_rcp_f32_e32 v54, v54
	v_mov_b32_e32 v55, 0
	v_mul_f32_e32 v63, v64, v63
	v_cvt_pk_fp8_f32 v55, v50, v51
	v_mul_f32_e32 v60, v63, v60
	v_mul_f32_e32 v50, v57, v54
	v_med3_f32 v60, v60, s46, v222
	v_mul_f32_e32 v50, v50, v53
	v_cvt_pk_fp8_f32 v62, v60, v61 op_sel:[0,0,1]
	v_med3_f32 v52, v52, s46, v222
	v_med3_f32 v50, v50, s46, v222
	v_cvt_pk_fp8_f32 v55, v52, v50 op_sel:[0,0,1]
	v_add_u32_e32 v50, v66, v103
	ds_write_b32 v50, v62
	v_add_u32_e32 v50, v66, v92
	ds_write_b32 v50, v55
	v_mul_f32_e32 v50, 0xbfb8aa3b, v46
	v_exp_f32_e32 v50, v50
	v_mul_f32_e32 v51, 0xbfb8aa3b, v47
	v_exp_f32_e32 v51, v51
	s_movk_i32 s53, 0x5000
	v_add_f32_e32 v50, 1.0, v50
	v_rcp_f32_e32 v50, v50
	v_add_f32_e32 v51, 1.0, v51
	v_rcp_f32_e32 v51, v51
	s_mov_b64 s[30:31], 0
	v_mul_f32_e32 v46, v46, v50
	v_mul_f32_e32 v38, v46, v38
	v_mul_f32_e32 v46, v47, v51
	v_mul_f32_e32 v39, v46, v39
	v_mul_f32_e32 v46, 0xbfb8aa3b, v49
	v_exp_f32_e32 v46, v46
	v_mul_f32_e32 v47, 0xbfb8aa3b, v48
	v_exp_f32_e32 v47, v47
	v_med3_f32 v38, v38, s46, v222
	v_add_f32_e32 v46, 1.0, v46
	v_rcp_f32_e32 v46, v46
	v_add_f32_e32 v47, 1.0, v47
	v_rcp_f32_e32 v47, v47
	v_med3_f32 v39, v39, s46, v222
	v_mul_f32_e32 v46, v49, v46
	v_mul_f32_e32 v41, v46, v41
	v_mov_b32_e32 v46, 0
	v_mul_f32_e32 v47, v48, v47
	v_cvt_pk_fp8_f32 v46, v38, v39
	v_mul_f32_e32 v38, 0xbfb8aa3b, v34
	v_mul_f32_e32 v40, v47, v40
	v_exp_f32_e32 v47, v38
	v_med3_f32 v40, v40, s46, v222
	v_med3_f32 v41, v41, s46, v222
	v_cvt_pk_fp8_f32 v46, v40, v41 op_sel:[0,0,1]
	v_add_f32_e32 v40, 1.0, v47
	v_pk_mul_f32 v[38:39], v[44:45], v[78:79] op_sel_hi:[1,0]
	v_rcp_f32_e32 v44, v40
	v_mul_f32_e32 v40, 0xbfb8aa3b, v35
	v_exp_f32_e32 v45, v40
	v_pk_mul_f32 v[40:41], v[42:43], v[78:79] op_sel_hi:[1,0]
	v_mul_f32_e32 v34, v34, v44
	v_mul_f32_e32 v34, v34, v40
	v_add_f32_e32 v40, 1.0, v45
	v_mul_f32_e32 v42, 0xbfb8aa3b, v36
	v_rcp_f32_e32 v40, v40
	v_exp_f32_e32 v42, v42
	v_med3_f32 v34, v34, s46, v222
	s_and_b64 vcc, exec, s[28:29]
	v_mul_f32_e32 v35, v35, v40
	v_add_f32_e32 v40, 1.0, v42
	v_mul_f32_e32 v35, v35, v41
	v_rcp_f32_e32 v40, v40
	v_mul_f32_e32 v41, 0xbfb8aa3b, v37
	v_exp_f32_e32 v41, v41
	v_med3_f32 v35, v35, s46, v222
	v_mul_f32_e32 v36, v36, v40
	v_mul_f32_e32 v36, v36, v38
	v_add_f32_e32 v38, 1.0, v41
	v_rcp_f32_e32 v38, v38
	v_mov_b32_e32 v40, 0
	v_cvt_pk_fp8_f32 v40, v34, v35
	v_med3_f32 v36, v36, s46, v222
	v_mul_f32_e32 v34, v37, v38
	v_mul_f32_e32 v34, v34, v39
	v_med3_f32 v34, v34, s46, v222
	v_cvt_pk_fp8_f32 v40, v36, v34 op_sel:[0,0,1]
	v_add_u32_e32 v34, v66, v84
	ds_write_b32 v34, v46
	v_add_u32_e32 v34, v66, v74
	ds_write_b32 v34, v40
	s_cbranch_vccz .LBB0_721
	s_waitcnt lgkmcnt(0)
	s_barrier
	s_add_i32 s1, 0, 0x14000
	v_and_b32_e32 v225, 15, v223
	v_ashrrev_i32_e32 v224, 4, v223
	v_lshlrev_b32_e32 v194, 5, v223
	v_lshl_add_u32 v196, v225, 8, s1
	v_lshlrev_b32_e32 v197, 1, v224
	s_mov_b32 s1, 0
	s_mov_b32 s28, 64
	s_mov_b32 s29, 0
	s_add_i32 s30, s29, 1
	s_bitcmp0_b32 s30, 1
	s_cselect_b32 s34, s49, s0
	s_lshr_b32 s29, s29, 1
	s_and_b32 s31, s1, 8
	s_mulk_i32 s29, 0x5000
	v_add_u32_e32 v114, s31, v197
	v_add_u32_e32 v115, s29, v196
	s_and_b32 s29, s28, 64
	s_and_b32 s31, s30, 12
	v_xor_b32_e32 v116, v114, v225
	v_bitop3_b32 v114, v114, v225, 1 bitop3:0x36
	s_ashr_i32 s35, s34, 31
	s_or_b32 s29, s29, s31
	v_lshl_add_u32 v134, v116, 4, v115
	v_lshl_add_u32 v135, v114, 4, v115
	s_lshl_b64 s[34:35], s[34:35], 18
	s_lshl_b32 s29, s29, 11
	ds_read_b128 v[118:121], v135
	ds_read_b128 v[114:117], v134
	ds_read_b128 v[122:125], v134 offset:4096
	ds_read_b128 v[130:133], v134 offset:16384
	ds_read_b128 v[126:129], v135 offset:4096
	ds_read_b128 v[142:145], v135 offset:8192
	ds_read_b128 v[138:141], v134 offset:8192
	ds_read_b128 v[146:149], v134 offset:12288
	ds_read_b128 v[150:153], v135 offset:12288
	ds_read_b128 v[134:137], v135 offset:16384
	s_add_u32 s31, s39, s34
	s_addc_u32 s35, s40, s35
	s_add_u32 s34, s31, s29
	s_addc_u32 s35, s35, 0
	v_lshl_add_u64 v[154:155], s[34:35], 0, v[194:195]
	s_waitcnt vmcnt(6) lgkmcnt(8)
	v_mfma_scale_f32_16x16x128_f8f6f4 v[110:113], v[2:9], v[114:121], 0, v220, v220 op_sel_hi:[0,0,0]
	s_waitcnt lgkmcnt(5)
	v_mfma_scale_f32_16x16x128_f8f6f4 v[106:109], v[2:9], v[122:129], 0, v220, v220 op_sel_hi:[0,0,0]
	s_waitcnt lgkmcnt(3)
; #define MX(a_, b_, c_) __builtin_amdgcn_mfma_scale_f32_16x16x128_f8f6f4(a_, b_, c_, 0, 0, 0, 0x7f7f7f7f, 0, 0x7f7f7f7f)
; #define LD32(p_) CAT8(*(const i32x4v*)(p_), *(const i32x4v*)((p_) + 16))
; #define AFRAG(mi_, ks_) CAT8(*(const i32x4v*)(smem + aoff + (mi_) * 16384 + (((8 * (ks_) + 2 * g) ^ lr) << 4)), *(const i32x4v*)(smem + aoff + (mi_) * 16384 + (((8 * (ks_) + 2 * g + 1) ^ lr) << 4)))
; #define AFRAG(hb_, mi_, ks_) CAT8(*(const i32x4v*)((hb_) + aoff + (mi_) * 4096 + (((8 * (ks_) + 2 * g2) ^ lr2) << 4)), *(const i32x4v*)((hb_) + aoff + (mi_) * 4096 + (((8 * (ks_) + 2 * g2 + 1) ^ lr2) << 4)))
; DEVINL void phase5(const Params& P, unsigned char* smem) {
;     ...
;                 for (int sk = 0; sk < 4; ++sk) {
;                     const int sn = 4 * ph + sk + 1 < 8 ? 4 * ph + sk + 1 : 7, sxn = (sn >> 1) & 1;
;                     const unsigned char* wn = wd0 + (size_t)(sxn ? e_hi : e_lo) * (2 * 64 * 2048) + (size_t)((sn & 1) * 64 + 4 * (sn >> 2)) * 2048;
;                     const unsigned char* hb = hs0 + (sk >> 1) * 20480;
;                     i32x8 fa[5];
; #pragma unroll
;                     for (int mi_ = 0; mi_ < 5; ++mi_) fa[mi_] = AFRAG(hb, mi_, sk & 1);
; #pragma unroll
;                     for (int j_ = 0; j_ < 4; ++j_) {
; #pragma unroll
;                         for (int mi_ = 0; mi_ < 5; ++mi_) acc[j_][mi_] = MX(b0[j_], fa[mi_], acc[j_][mi_]);
;                         b0[j_] = LD32(wn + j_ * 2048 + voff2);
;                         __builtin_amdgcn_sched_barrier(0);
;                     }
	v_mfma_scale_f32_16x16x128_f8f6f4 v[102:105], v[2:9], v[138:145], 0, v220, v220 op_sel_hi:[0,0,0]
	s_waitcnt lgkmcnt(1)
	v_mfma_scale_f32_16x16x128_f8f6f4 v[98:101], v[2:9], v[146:153], 0, v220, v220 op_sel_hi:[0,0,0]
	s_waitcnt lgkmcnt(0)
	v_mfma_scale_f32_16x16x128_f8f6f4 v[94:97], v[2:9], v[130:137], 0, v220, v220 op_sel_hi:[0,0,0]
	global_load_dwordx4 v[2:5], v[154:155], off
	global_load_dwordx4 v[6:9], v[154:155], off offset:16
	s_waitcnt vmcnt(6)
	v_mfma_scale_f32_16x16x128_f8f6f4 v[90:93], v[10:17], v[114:121], 0, v220, v220 op_sel_hi:[0,0,0]
	v_mfma_scale_f32_16x16x128_f8f6f4 v[86:89], v[10:17], v[122:129], 0, v220, v220 op_sel_hi:[0,0,0]
	v_mfma_scale_f32_16x16x128_f8f6f4 v[82:85], v[10:17], v[138:145], 0, v220, v220 op_sel_hi:[0,0,0]
	v_mfma_scale_f32_16x16x128_f8f6f4 v[78:81], v[10:17], v[146:153], 0, v220, v220 op_sel_hi:[0,0,0]
	v_mfma_scale_f32_16x16x128_f8f6f4 v[74:77], v[10:17], v[130:137], 0, v220, v220 op_sel_hi:[0,0,0]
	global_load_dwordx4 v[10:13], v[154:155], off offset:2048
	global_load_dwordx4 v[14:17], v[154:155], off offset:2064
	v_add_co_u32_e32 v158, vcc, s45, v154
	s_waitcnt vmcnt(6)
	v_mfma_scale_f32_16x16x128_f8f6f4 v[70:73], v[18:25], v[114:121], 0, v220, v220 op_sel_hi:[0,0,0]
	v_addc_co_u32_e32 v159, vcc, 0, v155, vcc
	v_lshl_add_u64 v[156:157], v[154:155], 0, s[14:15]
	v_mfma_scale_f32_16x16x128_f8f6f4 v[66:69], v[18:25], v[122:129], 0, v220, v220 op_sel_hi:[0,0,0]
	v_mfma_scale_f32_16x16x128_f8f6f4 v[62:65], v[18:25], v[138:145], 0, v220, v220 op_sel_hi:[0,0,0]
	v_mfma_scale_f32_16x16x128_f8f6f4 v[58:61], v[18:25], v[146:153], 0, v220, v220 op_sel_hi:[0,0,0]
	v_mfma_scale_f32_16x16x128_f8f6f4 v[54:57], v[18:25], v[130:137], 0, v220, v220 op_sel_hi:[0,0,0]
	global_load_dwordx4 v[18:21], v[158:159], off
	global_load_dwordx4 v[22:25], v[156:157], off offset:16
	s_waitcnt vmcnt(6)
	v_mfma_scale_f32_16x16x128_f8f6f4 v[50:53], v[26:33], v[114:121], 0, v220, v220 op_sel_hi:[0,0,0]
	v_lshl_add_u64 v[114:115], v[154:155], 0, s[16:17]
	v_mfma_scale_f32_16x16x128_f8f6f4 v[46:49], v[26:33], v[122:129], 0, v220, v220 op_sel_hi:[0,0,0]
	v_mfma_scale_f32_16x16x128_f8f6f4 v[42:45], v[26:33], v[138:145], 0, v220, v220 op_sel_hi:[0,0,0]
	v_mfma_scale_f32_16x16x128_f8f6f4 v[38:41], v[26:33], v[146:153], 0, v220, v220 op_sel_hi:[0,0,0]
	v_mfma_scale_f32_16x16x128_f8f6f4 v[34:37], v[26:33], v[130:137], 0, v220, v220 op_sel_hi:[0,0,0]
	global_load_dwordx4 v[26:29], v[158:159], off offset:2048
	global_load_dwordx4 v[30:33], v[114:115], off offset:16
	s_add_i32 s1, s1, 8
	s_add_i32 s28, s28, 64
	s_cmp_eq_u32 s30, 4
	s_mov_b32 s29, s30
.LBB0_725:
	s_add_i32 s30, s29, 1
	s_bitcmp0_b32 s30, 1
	s_cselect_b32 s34, s49, s0
	s_lshr_b32 s29, s29, 1
	s_and_b32 s31, s1, 8
	s_mulk_i32 s29, 0x5000
	v_add_u32_e32 v114, s31, v197
	v_add_u32_e32 v115, s29, v196
	s_and_b32 s29, s28, 64
	s_and_b32 s31, s30, 12
	v_xor_b32_e32 v116, v114, v225
	v_bitop3_b32 v114, v114, v225, 1 bitop3:0x36
	s_ashr_i32 s35, s34, 31
	s_or_b32 s29, s29, s31
	v_lshl_add_u32 v134, v116, 4, v115
	v_lshl_add_u32 v135, v114, 4, v115
	s_lshl_b64 s[34:35], s[34:35], 18
	s_lshl_b32 s29, s29, 11
	ds_read_b128 v[118:121], v135
	ds_read_b128 v[114:117], v134
	ds_read_b128 v[122:125], v134 offset:4096
	ds_read_b128 v[130:133], v134 offset:16384
	ds_read_b128 v[126:129], v135 offset:4096
	ds_read_b128 v[142:145], v135 offset:8192
	ds_read_b128 v[138:141], v134 offset:8192
	ds_read_b128 v[146:149], v134 offset:12288
	ds_read_b128 v[150:153], v135 offset:12288
	ds_read_b128 v[134:137], v135 offset:16384
	s_add_u32 s31, s39, s34
	s_addc_u32 s35, s40, s35
	s_add_u32 s34, s31, s29
	s_addc_u32 s35, s35, 0
	v_lshl_add_u64 v[154:155], s[34:35], 0, v[194:195]
	s_waitcnt vmcnt(6) lgkmcnt(8)
	v_mfma_scale_f32_16x16x128_f8f6f4 v[110:113], v[2:9], v[114:121], v[110:113], v220, v220 op_sel_hi:[0,0,0]
	s_waitcnt lgkmcnt(5)
	v_mfma_scale_f32_16x16x128_f8f6f4 v[106:109], v[2:9], v[122:129], v[106:109], v220, v220 op_sel_hi:[0,0,0]
	s_waitcnt lgkmcnt(3)
	v_mfma_scale_f32_16x16x128_f8f6f4 v[102:105], v[2:9], v[138:145], v[102:105], v220, v220 op_sel_hi:[0,0,0]
	s_waitcnt lgkmcnt(1)
	v_mfma_scale_f32_16x16x128_f8f6f4 v[98:101], v[2:9], v[146:153], v[98:101], v220, v220 op_sel_hi:[0,0,0]
	s_waitcnt lgkmcnt(0)
	v_mfma_scale_f32_16x16x128_f8f6f4 v[94:97], v[2:9], v[130:137], v[94:97], v220, v220 op_sel_hi:[0,0,0]
	global_load_dwordx4 v[2:5], v[154:155], off
	global_load_dwordx4 v[6:9], v[154:155], off offset:16
	s_waitcnt vmcnt(6)
	v_mfma_scale_f32_16x16x128_f8f6f4 v[90:93], v[10:17], v[114:121], v[90:93], v220, v220 op_sel_hi:[0,0,0]
	v_mfma_scale_f32_16x16x128_f8f6f4 v[86:89], v[10:17], v[122:129], v[86:89], v220, v220 op_sel_hi:[0,0,0]
	v_mfma_scale_f32_16x16x128_f8f6f4 v[82:85], v[10:17], v[138:145], v[82:85], v220, v220 op_sel_hi:[0,0,0]
	v_mfma_scale_f32_16x16x128_f8f6f4 v[78:81], v[10:17], v[146:153], v[78:81], v220, v220 op_sel_hi:[0,0,0]
	v_mfma_scale_f32_16x16x128_f8f6f4 v[74:77], v[10:17], v[130:137], v[74:77], v220, v220 op_sel_hi:[0,0,0]
	global_load_dwordx4 v[10:13], v[154:155], off offset:2048
	global_load_dwordx4 v[14:17], v[154:155], off offset:2064
	v_add_co_u32_e32 v158, vcc, s45, v154
	s_waitcnt vmcnt(6)
	v_mfma_scale_f32_16x16x128_f8f6f4 v[70:73], v[18:25], v[114:121], v[70:73], v220, v220 op_sel_hi:[0,0,0]
	v_addc_co_u32_e32 v159, vcc, 0, v155, vcc
	v_lshl_add_u64 v[156:157], v[154:155], 0, s[14:15]
	v_mfma_scale_f32_16x16x128_f8f6f4 v[66:69], v[18:25], v[122:129], v[66:69], v220, v220 op_sel_hi:[0,0,0]
	v_mfma_scale_f32_16x16x128_f8f6f4 v[62:65], v[18:25], v[138:145], v[62:65], v220, v220 op_sel_hi:[0,0,0]
	v_mfma_scale_f32_16x16x128_f8f6f4 v[58:61], v[18:25], v[146:153], v[58:61], v220, v220 op_sel_hi:[0,0,0]
	v_mfma_scale_f32_16x16x128_f8f6f4 v[54:57], v[18:25], v[130:137], v[54:57], v220, v220 op_sel_hi:[0,0,0]
	global_load_dwordx4 v[18:21], v[158:159], off
	global_load_dwordx4 v[22:25], v[156:157], off offset:16
	s_waitcnt vmcnt(6)
	v_mfma_scale_f32_16x16x128_f8f6f4 v[50:53], v[26:33], v[114:121], v[50:53], v220, v220 op_sel_hi:[0,0,0]
	v_lshl_add_u64 v[114:115], v[154:155], 0, s[16:17]
	v_mfma_scale_f32_16x16x128_f8f6f4 v[46:49], v[26:33], v[122:129], v[46:49], v220, v220 op_sel_hi:[0,0,0]
	v_mfma_scale_f32_16x16x128_f8f6f4 v[42:45], v[26:33], v[138:145], v[42:45], v220, v220 op_sel_hi:[0,0,0]
	v_mfma_scale_f32_16x16x128_f8f6f4 v[38:41], v[26:33], v[146:153], v[38:41], v220, v220 op_sel_hi:[0,0,0]
	v_mfma_scale_f32_16x16x128_f8f6f4 v[34:37], v[26:33], v[130:137], v[34:37], v220, v220 op_sel_hi:[0,0,0]
	global_load_dwordx4 v[26:29], v[158:159], off offset:2048
	global_load_dwordx4 v[30:33], v[114:115], off offset:16
	s_add_i32 s1, s1, 8
	s_add_i32 s28, s28, 64
	s_cmp_eq_u32 s30, 4
	s_mov_b32 s29, s30
	s_cbranch_scc0 .LBB0_725
; #define MX(a_, b_, c_) __builtin_amdgcn_mfma_scale_f32_16x16x128_f8f6f4(a_, b_, c_, 0, 0, 0, 0x7f7f7f7f, 0, 0x7f7f7f7f)
; #define LD32(p_) CAT8(*(const i32x4v*)(p_), *(const i32x4v*)((p_) + 16))
; #define AFRAG(mi_, ks_) CAT8(*(const i32x4v*)(smem + aoff + (mi_) * 16384 + (((8 * (ks_) + 2 * g) ^ lr) << 4)), *(const i32x4v*)(smem + aoff + (mi_) * 16384 + (((8 * (ks_) + 2 * g + 1) ^ lr) << 4)))
; #define AFRAG(hb_, mi_, ks_) CAT8(*(const i32x4v*)((hb_) + aoff + (mi_) * 4096 + (((8 * (ks_) + 2 * g2) ^ lr2) << 4)), *(const i32x4v*)((hb_) + aoff + (mi_) * 4096 + (((8 * (ks_) + 2 * g2 + 1) ^ lr2) << 4)))
; DEVINL void phase5(const Params& P, unsigned char* smem) {
;     ...
;             for (int ph = 0; ph < 2; ++ph) {
; #pragma unroll
;                 for (int i = 0; i < 4; ++i)
; #pragma unroll
;                     for (int mi = 0; mi < 5; ++mi) acc[i][mi] = (f32x4){0.f, 0.f, 0.f, 0.f};
; #pragma unroll 1
;                 for (int sk = 0; sk < 4; ++sk) {
;                     const int sn = 4 * ph + sk + 1 < 8 ? 4 * ph + sk + 1 : 7, sxn = (sn >> 1) & 1;
;                     const unsigned char* wn = wd0 + (size_t)(sxn ? e_hi : e_lo) * (2 * 64 * 2048) + (size_t)((sn & 1) * 64 + 4 * (sn >> 2)) * 2048;
;                     const unsigned char* hb = hs0 + (sk >> 1) * 20480;
;                     i32x8 fa[5];
; #pragma unroll
;                     for (int mi_ = 0; mi_ < 5; ++mi_) fa[mi_] = AFRAG(hb, mi_, sk & 1);
; #pragma unroll
;                     for (int j_ = 0; j_ < 4; ++j_) {
; #pragma unroll
;                         for (int mi_ = 0; mi_ < 5; ++mi_) acc[j_][mi_] = MX(b0[j_], fa[mi_], acc[j_][mi_]);
;                         b0[j_] = LD32(wn + j_ * 2048 + voff2);
;                         __builtin_amdgcn_sched_barrier(0);
;                     }
	s_mov_b32 s1, 0
	s_mov_b32 s28, 0
	s_min_u32 s29, s28, 2
	s_add_i32 s29, s29, 5
	s_bitcmp0_b32 s29, 1
	s_cselect_b32 s30, s49, s0
	s_lshr_b32 s31, s28, 1
	s_mulk_i32 s31, 0x5000
	s_and_b32 s34, s1, 8
	v_add_u32_e32 v199, s31, v196
	s_lshl_b32 s29, s29, 17
	s_ashr_i32 s31, s30, 31
	v_add_u32_e32 v198, s34, v197
	s_and_b32 s29, s29, 0x20000
	s_lshl_b64 s[30:31], s[30:31], 18
	v_xor_b32_e32 v200, v198, v225
	v_bitop3_b32 v198, v198, v225, 1 bitop3:0x36
	s_add_u32 s30, s39, s30
	v_lshl_add_u32 v214, v200, 4, v199
	v_lshl_add_u32 v215, v198, 4, v199
	s_addc_u32 s31, s40, s31
	ds_read_b128 v[202:205], v215
	ds_read_b128 v[198:201], v214
	ds_read_b128 v[206:209], v214 offset:4096
	ds_read_b128 v[226:229], v214 offset:16384
	ds_read_b128 v[210:213], v215 offset:4096
	ds_read_b128 v[238:241], v215 offset:8192
	ds_read_b128 v[234:237], v214 offset:8192
	ds_read_b128 v[242:245], v214 offset:12288
	ds_read_b128 v[246:249], v215 offset:12288
	ds_read_b128 v[230:233], v215 offset:16384
	s_add_u32 s30, s30, s29
	s_addc_u32 s31, s31, 0
	v_lshl_add_u64 v[214:215], s[30:31], 0, v[194:195]
	v_add_co_u32_e32 v218, vcc, s47, v214
	s_waitcnt vmcnt(6) lgkmcnt(8)
	v_mfma_scale_f32_16x16x128_f8f6f4 v[190:193], v[2:9], v[198:205], 0, v220, v220 op_sel_hi:[0,0,0]
	v_addc_co_u32_e32 v219, vcc, 0, v215, vcc
	v_lshl_add_u64 v[216:217], v[214:215], 0, s[20:21]
	s_waitcnt lgkmcnt(5)
	v_mfma_scale_f32_16x16x128_f8f6f4 v[186:189], v[2:9], v[206:213], 0, v220, v220 op_sel_hi:[0,0,0]
	s_waitcnt lgkmcnt(3)
	v_mfma_scale_f32_16x16x128_f8f6f4 v[182:185], v[2:9], v[234:241], 0, v220, v220 op_sel_hi:[0,0,0]
	s_waitcnt lgkmcnt(1)
	v_mfma_scale_f32_16x16x128_f8f6f4 v[178:181], v[2:9], v[242:249], 0, v220, v220 op_sel_hi:[0,0,0]
	s_waitcnt lgkmcnt(0)
	v_mfma_scale_f32_16x16x128_f8f6f4 v[174:177], v[2:9], v[226:233], 0, v220, v220 op_sel_hi:[0,0,0]
	global_load_dwordx4 v[2:5], v[218:219], off offset:-4096
	global_load_dwordx4 v[6:9], v[216:217], off offset:16
	s_waitcnt vmcnt(6)
	v_mfma_scale_f32_16x16x128_f8f6f4 v[170:173], v[10:17], v[198:205], 0, v220, v220 op_sel_hi:[0,0,0]
	v_mfma_scale_f32_16x16x128_f8f6f4 v[166:169], v[10:17], v[206:213], 0, v220, v220 op_sel_hi:[0,0,0]
	v_mfma_scale_f32_16x16x128_f8f6f4 v[162:165], v[10:17], v[234:241], 0, v220, v220 op_sel_hi:[0,0,0]
	v_mfma_scale_f32_16x16x128_f8f6f4 v[158:161], v[10:17], v[242:249], 0, v220, v220 op_sel_hi:[0,0,0]
	v_mfma_scale_f32_16x16x128_f8f6f4 v[154:157], v[10:17], v[226:233], 0, v220, v220 op_sel_hi:[0,0,0]
	global_load_dwordx4 v[10:13], v[216:217], off offset:2048
	global_load_dwordx4 v[14:17], v[216:217], off offset:2064
	s_waitcnt vmcnt(6)
	v_mfma_scale_f32_16x16x128_f8f6f4 v[150:153], v[18:25], v[198:205], 0, v220, v220 op_sel_hi:[0,0,0]
	v_lshl_add_u64 v[216:217], v[214:215], 0, s[22:23]
	v_mfma_scale_f32_16x16x128_f8f6f4 v[146:149], v[18:25], v[206:213], 0, v220, v220 op_sel_hi:[0,0,0]
	v_mfma_scale_f32_16x16x128_f8f6f4 v[142:145], v[18:25], v[234:241], 0, v220, v220 op_sel_hi:[0,0,0]
	v_mfma_scale_f32_16x16x128_f8f6f4 v[138:141], v[18:25], v[242:249], 0, v220, v220 op_sel_hi:[0,0,0]
	v_mfma_scale_f32_16x16x128_f8f6f4 v[134:137], v[18:25], v[226:233], 0, v220, v220 op_sel_hi:[0,0,0]
	global_load_dwordx4 v[18:21], v[218:219], off
	global_load_dwordx4 v[22:25], v[216:217], off offset:16
	s_waitcnt vmcnt(6)
	v_mfma_scale_f32_16x16x128_f8f6f4 v[130:133], v[26:33], v[198:205], 0, v220, v220 op_sel_hi:[0,0,0]
	v_lshl_add_u64 v[198:199], v[214:215], 0, s[24:25]
	v_mfma_scale_f32_16x16x128_f8f6f4 v[126:129], v[26:33], v[206:213], 0, v220, v220 op_sel_hi:[0,0,0]
	v_mfma_scale_f32_16x16x128_f8f6f4 v[122:125], v[26:33], v[234:241], 0, v220, v220 op_sel_hi:[0,0,0]
	v_mfma_scale_f32_16x16x128_f8f6f4 v[118:121], v[26:33], v[242:249], 0, v220, v220 op_sel_hi:[0,0,0]
	v_mfma_scale_f32_16x16x128_f8f6f4 v[114:117], v[26:33], v[226:233], 0, v220, v220 op_sel_hi:[0,0,0]
	global_load_dwordx4 v[26:29], v[218:219], off offset:2048
	global_load_dwordx4 v[30:33], v[198:199], off offset:16
	s_add_i32 s28, s28, 1
	s_add_i32 s1, s1, 8
	s_cmp_lg_u32 s28, 4
